# N1 row-norm reductions: ds_bpermute butterflies replaced by DPP moves and permlane swaps (same add order)
# speedup vs baseline: 1.0039x; 1.0039x over previous
; #define GAS __attribute__((address_space(1)))
; __device__ __forceinline__ unsigned pk2(float lo, float hi) { unsigned r; asm("v_cvt_pk_bf16_f32 %0, %1, %2" : "=v"(r) : "v"(lo), "v"(hi)); return r; }
; __device__ __forceinline__ bf16_t* x_row_ptr(Frame& F, int row) { return (bf16_t*)(F.ws + WS_X) + (size_t)row * D; }
; __device__ __forceinline__ float wave_sum(float v) {
; #pragma unroll
;     for (int o = 1; o < 64; o <<= 1) v += __shfl_xor(v, o);
;     return v;
; }
; __device__ __forceinline__ void n1_finish16(Frame& F, int L, int row, const f32x4 (&v)[4], const f32x4 (&gs)[4], const f32x4 (&sh)[4]) {
;     { GAS u32x4* xo = (GAS u32x4*)x_row_ptr(F, row) + 2 * F.lane;
; #pragma unroll
;       for (int h = 0; h < 2; ++h) { u32x4 w; w.x = pk2(v[2 * h][0], v[2 * h][1]); w.y = pk2(v[2 * h][2], v[2 * h][3]); w.z = pk2(v[2 * h + 1][0], v[2 * h + 1][1]); w.w = pk2(v[2 * h + 1][2], v[2 * h + 1][3]); xo[h] = w; } }
;     float ss = 0.f;
; #pragma unroll
;     for (int j = 0; j < 4; ++j) ss += (v[j][0] * v[j][0] + v[j][1] * v[j][1]) + (v[j][2] * v[j][2] + v[j][3] * v[j][3]);
;     const float rinv = __builtin_amdgcn_rsqf(wave_sum(ss) * (1.0f / D) + EPS);
;     if ((L & 1) == 0) {
;         u32x4 o;
; #pragma unroll
;         for (int q = 0; q < 4; ++q) { const f32x4 h = ((v[q] * rinv) * gs[q] + sh[q]) * pg8::SC_H2; o[q] = pg8::pack4_fp8(h[0], h[1], h[2], h[3]); }
;         *((GAS u32x4*)((unsigned char*)(F.ws + WS_H) + (size_t)row * D) + F.lane) = o;
;     } else {
;         GAS u32x4* ho = (GAS u32x4*)((bf16_t*)(F.ws + WS_H) + (size_t)row * D) + 2 * F.lane;
; #pragma unroll
;         for (int hh = 0; hh < 2; ++hh) { const f32x4 h0 = (v[2 * hh] * rinv) * gs[2 * hh] + sh[2 * hh], h1 = (v[2 * hh + 1] * rinv) * gs[2 * hh + 1] + sh[2 * hh + 1];
;             u32x4 w; w.x = pk2(h0[0], h0[1]); w.y = pk2(h0[2], h0[3]); w.z = pk2(h1[0], h1[1]); w.w = pk2(h1[2], h1[3]); ho[hh] = w; }
.LBB0_234:
	s_ashr_i32 s5, s4, 31
	s_lshl_b64 s[0:1], s[4:5], 11
	s_waitcnt vmcnt(21)
	v_lshl_add_u64 v[78:79], v[160:161], 0, s[0:1]
	s_waitcnt vmcnt(20)
	v_cvt_pk_bf16_f32 v62, v172, v173
	v_cvt_pk_bf16_f32 v63, v174, v175
	v_cvt_pk_bf16_f32 v64, v168, v169
	v_cvt_pk_bf16_f32 v65, v170, v171
	global_store_dwordx4 v[78:79], v[62:65], off
	s_mov_b64 s[2:3], -1
	s_nop 0
	v_cvt_pk_bf16_f32 v62, v110, v111
	v_cvt_pk_bf16_f32 v63, v112, v113
	v_cvt_pk_bf16_f32 v64, v106, v107
	v_cvt_pk_bf16_f32 v65, v108, v109
	global_store_dwordx4 v[78:79], v[62:65], off offset:16
	s_nop 1
	v_mul_f32_e32 v62, v173, v173
	v_mul_f32_e32 v63, v175, v175
	v_fmac_f32_e32 v62, v172, v172
	v_fmac_f32_e32 v63, v174, v174
	v_add_f32_e32 v62, v62, v63
	v_mul_f32_e32 v63, v169, v169
	v_mul_f32_e32 v64, v171, v171
	v_fmac_f32_e32 v63, v168, v168
	v_fmac_f32_e32 v64, v170, v170
	v_add_f32_e32 v63, v63, v64
	v_add_f32_e32 v62, v63, v62
	v_mul_f32_e32 v63, v111, v111
	v_mul_f32_e32 v64, v113, v113
	v_fmac_f32_e32 v63, v110, v110
	v_fmac_f32_e32 v64, v112, v112
	v_add_f32_e32 v63, v63, v64
	v_add_f32_e32 v62, v63, v62
	v_mul_f32_e32 v63, v107, v107
	v_mul_f32_e32 v64, v109, v109
	v_fmac_f32_e32 v63, v106, v106
	v_fmac_f32_e32 v64, v108, v108
	v_add_f32_e32 v63, v63, v64
	v_add_f32_e32 v62, v63, v62
	v_and_b32_e32 v63, 64, v211
	v_add_u32_e32 v63, 64, v63
	v_xor_b32_e32 v64, 1, v211
	v_cmp_lt_i32_e32 vcc, v64, v63
	s_nop 1
	v_cndmask_b32_e32 v64, v211, v64, vcc
	v_lshlrev_b32_e32 v157, 2, v64
	s_waitcnt lgkmcnt(0)
	s_nop 1
	v_mov_b32_dpp v64, v62 quad_perm:[1,0,3,2] row_mask:0xf bank_mask:0xf
	v_add_f32_e32 v62, v62, v64
	v_xor_b32_e32 v64, 2, v211
	v_cmp_lt_i32_e32 vcc, v64, v63
	s_nop 1
	v_cndmask_b32_e32 v64, v211, v64, vcc
	v_lshlrev_b32_e32 v179, 2, v64
	s_waitcnt lgkmcnt(0)
	s_nop 1
	v_mov_b32_dpp v64, v62 quad_perm:[2,3,0,1] row_mask:0xf bank_mask:0xf
	v_add_f32_e32 v62, v62, v64
	v_xor_b32_e32 v64, 4, v211
	v_cmp_lt_i32_e32 vcc, v64, v63
	s_nop 1
	v_cndmask_b32_e32 v64, v211, v64, vcc
	v_lshlrev_b32_e32 v180, 2, v64
	s_waitcnt lgkmcnt(0)
	s_nop 1
	v_mov_b32_dpp v64, v62 row_half_mirror row_mask:0xf bank_mask:0xf
	v_add_f32_e32 v62, v62, v64
	v_xor_b32_e32 v64, 8, v211
	v_cmp_lt_i32_e32 vcc, v64, v63
	s_nop 1
	v_cndmask_b32_e32 v64, v211, v64, vcc
	v_lshlrev_b32_e32 v181, 2, v64
	s_waitcnt lgkmcnt(0)
	s_nop 1
	v_mov_b32_dpp v64, v62 row_mirror row_mask:0xf bank_mask:0xf
	v_add_f32_e32 v62, v62, v64
	v_xor_b32_e32 v64, 16, v211
	v_cmp_lt_i32_e32 vcc, v64, v63
	s_nop 1
	v_cndmask_b32_e32 v64, v211, v64, vcc
	v_lshlrev_b32_e32 v182, 2, v64
	s_waitcnt lgkmcnt(0)
	v_mov_b32_e32 v64, v62
	s_nop 1
	v_permlane16_swap_b32_e32 v64, v62
	v_add_f32_e32 v62, v62, v64
	v_xor_b32_e32 v64, 32, v211
	v_cmp_lt_i32_e32 vcc, v64, v63
	s_nop 1
	v_cndmask_b32_e32 v63, v211, v64, vcc
	v_lshlrev_b32_e32 v183, 2, v63
	s_and_b64 vcc, exec, s[48:49]
	s_waitcnt lgkmcnt(0)
	v_mov_b32_e32 v63, v62
	s_nop 1
	v_permlane32_swap_b32_e32 v63, v62
	v_add_f32_e32 v62, v62, v63
	v_fmamk_f32 v62, v62, 0x3a800000, v250
	v_rsq_f32_e32 v62, v62
	s_cbranch_vccz .LBB0_236
	v_pk_mul_f32 v[78:79], v[62:63], v[174:175] op_sel_hi:[0,1]
	v_pk_mul_f32 v[80:81], v[62:63], v[172:173] op_sel_hi:[0,1]
	v_pk_fma_f32 v[82:83], v[20:21], v[78:79], v[16:17]
	v_pk_fma_f32 v[78:79], v[18:19], v[80:81], v[14:15]
	v_pk_mul_f32 v[80:81], v[62:63], v[170:171] op_sel_hi:[0,1]
	v_pk_mul_f32 v[84:85], v[62:63], v[168:169] op_sel_hi:[0,1]
	v_pk_fma_f32 v[86:87], v[24:25], v[80:81], v[12:13]
	v_pk_fma_f32 v[80:81], v[22:23], v[84:85], v[10:11]
	v_lshl_add_u64 v[64:65], v[162:163], 0, s[0:1]
	v_cvt_pk_bf16_f32 v78, v78, v79
	v_cvt_pk_bf16_f32 v79, v82, v83
	v_cvt_pk_bf16_f32 v80, v80, v81
	v_cvt_pk_bf16_f32 v81, v86, v87
	global_store_dwordx4 v[64:65], v[78:81], off
	v_pk_mul_f32 v[84:85], v[62:63], v[106:107] op_sel_hi:[0,1]
	s_mov_b64 s[2:3], 0
	v_pk_mul_f32 v[78:79], v[62:63], v[112:113] op_sel_hi:[0,1]
	v_pk_mul_f32 v[80:81], v[62:63], v[110:111] op_sel_hi:[0,1]
	v_pk_fma_f32 v[82:83], v[28:29], v[78:79], v[8:9]
	v_pk_fma_f32 v[78:79], v[26:27], v[80:81], v[6:7]
	v_pk_mul_f32 v[80:81], v[62:63], v[108:109] op_sel_hi:[0,1]
	v_pk_fma_f32 v[86:87], v[32:33], v[80:81], v[4:5]
	v_pk_fma_f32 v[80:81], v[30:31], v[84:85], v[2:3]
	v_cvt_pk_bf16_f32 v78, v78, v79
	v_cvt_pk_bf16_f32 v79, v82, v83
	s_nop 0
	v_cvt_pk_bf16_f32 v80, v80, v81
	v_cvt_pk_bf16_f32 v81, v86, v87
	global_store_dwordx4 v[64:65], v[78:81], off offset:16

; #define GAS __attribute__((address_space(1)))
; __device__ __forceinline__ unsigned pk2(float lo, float hi) { unsigned r; asm("v_cvt_pk_bf16_f32 %0, %1, %2" : "=v"(r) : "v"(lo), "v"(hi)); return r; }
; __device__ __forceinline__ bf16_t* x_row_ptr(Frame& F, int row) { return (bf16_t*)(F.ws + WS_X) + (size_t)row * D; }
; __device__ __forceinline__ float wave_sum(float v) {
; #pragma unroll
;     for (int o = 1; o < 64; o <<= 1) v += __shfl_xor(v, o);
;     return v;
; }
; __device__ __forceinline__ void n1_finish16(Frame& F, int L, int row, const f32x4 (&v)[4], const f32x4 (&gs)[4], const f32x4 (&sh)[4]) {
;     { GAS u32x4* xo = (GAS u32x4*)x_row_ptr(F, row) + 2 * F.lane;
; #pragma unroll
;       for (int h = 0; h < 2; ++h) { u32x4 w; w.x = pk2(v[2 * h][0], v[2 * h][1]); w.y = pk2(v[2 * h][2], v[2 * h][3]); w.z = pk2(v[2 * h + 1][0], v[2 * h + 1][1]); w.w = pk2(v[2 * h + 1][2], v[2 * h + 1][3]); xo[h] = w; } }
;     float ss = 0.f;
; #pragma unroll
;     for (int j = 0; j < 4; ++j) ss += (v[j][0] * v[j][0] + v[j][1] * v[j][1]) + (v[j][2] * v[j][2] + v[j][3] * v[j][3]);
;     const float rinv = __builtin_amdgcn_rsqf(wave_sum(ss) * (1.0f / D) + EPS);
;     if ((L & 1) == 0) {
;         u32x4 o;
; #pragma unroll
;         for (int q = 0; q < 4; ++q) { const f32x4 h = ((v[q] * rinv) * gs[q] + sh[q]) * pg8::SC_H2; o[q] = pg8::pack4_fp8(h[0], h[1], h[2], h[3]); }
;         *((GAS u32x4*)((unsigned char*)(F.ws + WS_H) + (size_t)row * D) + F.lane) = o;
;     } else {
;         GAS u32x4* ho = (GAS u32x4*)((bf16_t*)(F.ws + WS_H) + (size_t)row * D) + 2 * F.lane;
; #pragma unroll
;         for (int hh = 0; hh < 2; ++hh) { const f32x4 h0 = (v[2 * hh] * rinv) * gs[2 * hh] + sh[2 * hh], h1 = (v[2 * hh + 1] * rinv) * gs[2 * hh + 1] + sh[2 * hh + 1];
;             u32x4 w; w.x = pk2(h0[0], h0[1]); w.y = pk2(h0[2], h0[3]); w.z = pk2(h1[0], h1[1]); w.w = pk2(h1[2], h1[3]); ho[hh] = w; }
.LBB0_261:
	s_ashr_i32 s87, s86, 31
	s_lshl_b64 s[2:3], s[86:87], 11
	s_waitcnt vmcnt(23)
	v_lshl_add_u64 v[38:39], v[160:161], 0, s[2:3]
	s_waitcnt vmcnt(22)
	v_cvt_pk_bf16_f32 v34, v172, v173
	v_cvt_pk_bf16_f32 v35, v174, v175
	v_cvt_pk_bf16_f32 v36, v168, v169
	v_cvt_pk_bf16_f32 v37, v170, v171
	global_store_dwordx4 v[38:39], v[34:37], off
	s_mov_b64 s[6:7], -1
	s_and_b64 vcc, exec, s[48:49]
	v_cvt_pk_bf16_f32 v34, v74, v75
	v_cvt_pk_bf16_f32 v35, v76, v77
	v_cvt_pk_bf16_f32 v36, v70, v71
	v_cvt_pk_bf16_f32 v37, v72, v73
	global_store_dwordx4 v[38:39], v[34:37], off offset:16
	s_nop 1
	v_mul_f32_e32 v34, v173, v173
	v_mul_f32_e32 v35, v175, v175
	v_fmac_f32_e32 v34, v172, v172
	v_fmac_f32_e32 v35, v174, v174
	v_add_f32_e32 v34, v34, v35
	v_mul_f32_e32 v35, v169, v169
	v_mul_f32_e32 v36, v171, v171
	v_fmac_f32_e32 v35, v168, v168
	v_fmac_f32_e32 v36, v170, v170
	v_add_f32_e32 v35, v35, v36
	v_add_f32_e32 v34, v35, v34
	v_mul_f32_e32 v35, v75, v75
	v_mul_f32_e32 v36, v77, v77
	v_fmac_f32_e32 v35, v74, v74
	v_fmac_f32_e32 v36, v76, v76
	v_add_f32_e32 v35, v35, v36
	v_add_f32_e32 v34, v35, v34
	v_mul_f32_e32 v35, v71, v71
	v_mul_f32_e32 v36, v73, v73
	v_fmac_f32_e32 v35, v70, v70
	v_fmac_f32_e32 v36, v72, v72
	v_add_f32_e32 v35, v35, v36
	v_add_f32_e32 v34, v35, v34
	s_waitcnt lgkmcnt(0)
	s_nop 1
	v_mov_b32_dpp v35, v34 quad_perm:[1,0,3,2] row_mask:0xf bank_mask:0xf
	v_add_f32_e32 v34, v34, v35
	s_waitcnt lgkmcnt(0)
	s_nop 1
	v_mov_b32_dpp v35, v34 quad_perm:[2,3,0,1] row_mask:0xf bank_mask:0xf
	v_add_f32_e32 v34, v34, v35
	s_waitcnt lgkmcnt(0)
	s_nop 1
	v_mov_b32_dpp v35, v34 row_half_mirror row_mask:0xf bank_mask:0xf
	v_add_f32_e32 v34, v34, v35
	s_waitcnt lgkmcnt(0)
	s_nop 1
	v_mov_b32_dpp v35, v34 row_mirror row_mask:0xf bank_mask:0xf
	v_add_f32_e32 v34, v34, v35
	s_waitcnt lgkmcnt(0)
	v_mov_b32_e32 v35, v34
	s_nop 1
	v_permlane16_swap_b32_e32 v35, v34
	v_add_f32_e32 v34, v34, v35
	s_waitcnt lgkmcnt(0)
	v_mov_b32_e32 v35, v34
	s_nop 1
	v_permlane32_swap_b32_e32 v35, v34
	v_add_f32_e32 v34, v34, v35
	v_fmamk_f32 v34, v34, 0x3a800000, v250
	v_rsq_f32_e32 v34, v34
	s_cbranch_vccz .LBB0_291
	v_pk_mul_f32 v[36:37], v[34:35], v[174:175] op_sel_hi:[0,1]
	v_pk_mul_f32 v[38:39], v[34:35], v[172:173] op_sel_hi:[0,1]
	v_pk_fma_f32 v[42:43], v[20:21], v[36:37], v[16:17]
	v_pk_fma_f32 v[36:37], v[18:19], v[38:39], v[14:15]
	v_pk_mul_f32 v[38:39], v[34:35], v[170:171] op_sel_hi:[0,1]
	v_pk_mul_f32 v[44:45], v[34:35], v[168:169] op_sel_hi:[0,1]
	v_pk_fma_f32 v[46:47], v[24:25], v[38:39], v[12:13]
	v_pk_fma_f32 v[38:39], v[22:23], v[44:45], v[10:11]
	v_lshl_add_u64 v[40:41], v[162:163], 0, s[2:3]
	v_cvt_pk_bf16_f32 v36, v36, v37
	v_cvt_pk_bf16_f32 v37, v42, v43
	v_cvt_pk_bf16_f32 v38, v38, v39
	v_cvt_pk_bf16_f32 v39, v46, v47
	global_store_dwordx4 v[40:41], v[36:39], off
	v_pk_mul_f32 v[44:45], v[34:35], v[70:71] op_sel_hi:[0,1]
	s_nop 0
	v_pk_mul_f32 v[36:37], v[34:35], v[76:77] op_sel_hi:[0,1]
	v_pk_mul_f32 v[38:39], v[34:35], v[74:75] op_sel_hi:[0,1]
	v_pk_fma_f32 v[42:43], v[28:29], v[36:37], v[8:9]
	v_pk_fma_f32 v[36:37], v[26:27], v[38:39], v[6:7]
	v_pk_mul_f32 v[38:39], v[34:35], v[72:73] op_sel_hi:[0,1]
	v_pk_fma_f32 v[46:47], v[32:33], v[38:39], v[4:5]
	v_pk_fma_f32 v[38:39], v[30:31], v[44:45], v[2:3]
	v_cvt_pk_bf16_f32 v36, v36, v37
	v_cvt_pk_bf16_f32 v37, v42, v43
	s_nop 0
	v_cvt_pk_bf16_f32 v38, v38, v39
	v_cvt_pk_bf16_f32 v39, v46, v47
	global_store_dwordx4 v[40:41], v[36:39], off offset:16
	s_cbranch_execz .LBB0_292

; #define GAS __attribute__((address_space(1)))
; __device__ __forceinline__ unsigned pk2(float lo, float hi) { unsigned r; asm("v_cvt_pk_bf16_f32 %0, %1, %2" : "=v"(r) : "v"(lo), "v"(hi)); return r; }
; __device__ __forceinline__ bf16_t* x_row_ptr(Frame& F, int row) { return (bf16_t*)(F.ws + WS_X) + (size_t)row * D; }
; __device__ __forceinline__ float wave_sum(float v) {
; #pragma unroll
;     for (int o = 1; o < 64; o <<= 1) v += __shfl_xor(v, o);
;     return v;
; }
; __device__ __forceinline__ void n1_finish16(Frame& F, int L, int row, const f32x4 (&v)[4], const f32x4 (&gs)[4], const f32x4 (&sh)[4]) {
;     { GAS u32x4* xo = (GAS u32x4*)x_row_ptr(F, row) + 2 * F.lane;
; #pragma unroll
;       for (int h = 0; h < 2; ++h) { u32x4 w; w.x = pk2(v[2 * h][0], v[2 * h][1]); w.y = pk2(v[2 * h][2], v[2 * h][3]); w.z = pk2(v[2 * h + 1][0], v[2 * h + 1][1]); w.w = pk2(v[2 * h + 1][2], v[2 * h + 1][3]); xo[h] = w; } }
;     float ss = 0.f;
; #pragma unroll
;     for (int j = 0; j < 4; ++j) ss += (v[j][0] * v[j][0] + v[j][1] * v[j][1]) + (v[j][2] * v[j][2] + v[j][3] * v[j][3]);
;     const float rinv = __builtin_amdgcn_rsqf(wave_sum(ss) * (1.0f / D) + EPS);
;     if ((L & 1) == 0) {
;         u32x4 o;
; #pragma unroll
;         for (int q = 0; q < 4; ++q) { const f32x4 h = ((v[q] * rinv) * gs[q] + sh[q]) * pg8::SC_H2; o[q] = pg8::pack4_fp8(h[0], h[1], h[2], h[3]); }
;         *((GAS u32x4*)((unsigned char*)(F.ws + WS_H) + (size_t)row * D) + F.lane) = o;
;     } else {
;         GAS u32x4* ho = (GAS u32x4*)((bf16_t*)(F.ws + WS_H) + (size_t)row * D) + 2 * F.lane;
; #pragma unroll
;         for (int hh = 0; hh < 2; ++hh) { const f32x4 h0 = (v[2 * hh] * rinv) * gs[2 * hh] + sh[2 * hh], h1 = (v[2 * hh + 1] * rinv) * gs[2 * hh + 1] + sh[2 * hh + 1];
;             u32x4 w; w.x = pk2(h0[0], h0[1]); w.y = pk2(h0[2], h0[3]); w.z = pk2(h1[0], h1[1]); w.w = pk2(h1[2], h1[3]); ho[hh] = w; }
.LBB0_285:
	s_waitcnt vmcnt(24)
	v_mul_f32_e32 v114, v173, v173
	v_mul_f32_e32 v115, v175, v175
	v_fmac_f32_e32 v114, v172, v172
	v_fmac_f32_e32 v115, v174, v174
	v_add_f32_e32 v114, v114, v115
	v_mul_f32_e32 v115, v169, v169
	v_mul_f32_e32 v116, v171, v171
	v_fmac_f32_e32 v115, v168, v168
	v_fmac_f32_e32 v116, v170, v170
	v_add_f32_e32 v115, v115, v116
	v_add_f32_e32 v114, v115, v114
	v_mul_f32_e32 v115, v151, v151
	v_mul_f32_e32 v116, v153, v153
	v_fmac_f32_e32 v115, v150, v150
	v_fmac_f32_e32 v116, v152, v152
	v_add_f32_e32 v115, v115, v116
	v_add_f32_e32 v114, v115, v114
	v_mul_f32_e32 v115, v147, v147
	v_mul_f32_e32 v116, v149, v149
	v_fmac_f32_e32 v115, v146, v146
	v_fmac_f32_e32 v116, v148, v148
	v_add_f32_e32 v115, v115, v116
	v_add_f32_e32 v114, v115, v114
	s_mov_b64 s[18:19], -1
	s_and_b64 vcc, exec, s[48:49]
	s_waitcnt lgkmcnt(0)
	s_nop 1
	v_mov_b32_dpp v115, v114 quad_perm:[1,0,3,2] row_mask:0xf bank_mask:0xf
	v_add_f32_e32 v114, v114, v115
	s_waitcnt lgkmcnt(0)
	s_nop 1
	v_mov_b32_dpp v115, v114 quad_perm:[2,3,0,1] row_mask:0xf bank_mask:0xf
	v_add_f32_e32 v114, v114, v115
	s_waitcnt lgkmcnt(0)
	s_nop 1
	v_mov_b32_dpp v115, v114 row_half_mirror row_mask:0xf bank_mask:0xf
	v_add_f32_e32 v116, v114, v115
	v_cvt_pk_bf16_f32 v114, v172, v173
	v_cvt_pk_bf16_f32 v115, v174, v175
	s_waitcnt lgkmcnt(0)
	s_nop 1
	v_mov_b32_dpp v117, v116 row_mirror row_mask:0xf bank_mask:0xf
	v_add_f32_e32 v118, v116, v117
	v_cvt_pk_bf16_f32 v116, v168, v169
	v_cvt_pk_bf16_f32 v117, v170, v171
	global_store_dwordx4 v[166:167], v[114:117], off
	s_waitcnt lgkmcnt(0)
	v_mov_b32_e32 v119, v118
	s_nop 1
	v_permlane16_swap_b32_e32 v119, v118
	v_add_f32_e32 v118, v118, v119
	v_cvt_pk_bf16_f32 v114, v150, v151
	v_cvt_pk_bf16_f32 v115, v152, v153
	v_cvt_pk_bf16_f32 v116, v146, v147
	v_cvt_pk_bf16_f32 v117, v148, v149
	global_store_dwordx4 v[166:167], v[114:117], off offset:16
	s_waitcnt lgkmcnt(0)
	s_nop 0
	v_mov_b32_e32 v119, v118
	v_mov_b32_e32 v114, v118
	s_nop 1
	v_permlane32_swap_b32_e32 v119, v114
	v_add_f32_e32 v114, v114, v119
	v_fmamk_f32 v114, v114, 0x3a800000, v250
	v_rsq_f32_e32 v114, v114
	s_cbranch_vccz .LBB0_287
	v_pk_mul_f32 v[116:117], v[114:115], v[174:175] op_sel_hi:[0,1]
	v_pk_mul_f32 v[118:119], v[114:115], v[172:173] op_sel_hi:[0,1]
	v_readlane_b32 s18, v255, 26
	v_pk_fma_f32 v[122:123], v[20:21], v[116:117], v[16:17]
	v_pk_fma_f32 v[116:117], v[18:19], v[118:119], v[14:15]
	v_pk_mul_f32 v[118:119], v[114:115], v[170:171] op_sel_hi:[0,1]
	v_pk_mul_f32 v[124:125], v[114:115], v[168:169] op_sel_hi:[0,1]
	v_readlane_b32 s19, v255, 27
	v_pk_fma_f32 v[126:127], v[24:25], v[118:119], v[12:13]
	v_pk_fma_f32 v[118:119], v[22:23], v[124:125], v[10:11]
	v_lshl_add_u64 v[120:121], v[162:163], 0, s[18:19]
	v_cvt_pk_bf16_f32 v116, v116, v117
	v_cvt_pk_bf16_f32 v117, v122, v123
	v_cvt_pk_bf16_f32 v118, v118, v119
	v_cvt_pk_bf16_f32 v119, v126, v127
	global_store_dwordx4 v[120:121], v[116:119], off
	v_pk_mul_f32 v[124:125], v[114:115], v[146:147] op_sel_hi:[0,1]
	s_mov_b64 s[18:19], 0
	v_pk_mul_f32 v[116:117], v[114:115], v[152:153] op_sel_hi:[0,1]
	v_pk_mul_f32 v[118:119], v[114:115], v[150:151] op_sel_hi:[0,1]
	v_pk_fma_f32 v[122:123], v[28:29], v[116:117], v[8:9]
	v_pk_fma_f32 v[116:117], v[26:27], v[118:119], v[6:7]
	v_pk_mul_f32 v[118:119], v[114:115], v[148:149] op_sel_hi:[0,1]
	v_pk_fma_f32 v[126:127], v[32:33], v[118:119], v[4:5]
	v_pk_fma_f32 v[118:119], v[30:31], v[124:125], v[2:3]
	v_cvt_pk_bf16_f32 v116, v116, v117
	v_cvt_pk_bf16_f32 v117, v122, v123
	s_nop 0
	v_cvt_pk_bf16_f32 v118, v118, v119
	v_cvt_pk_bf16_f32 v119, v126, v127
	global_store_dwordx4 v[120:121], v[116:119], off offset:16

; #define GAS __attribute__((address_space(1)))
; __device__ __forceinline__ unsigned pk2(float lo, float hi) { unsigned r; asm("v_cvt_pk_bf16_f32 %0, %1, %2" : "=v"(r) : "v"(lo), "v"(hi)); return r; }
; __device__ __forceinline__ bf16_t* x_row_ptr(Frame& F, int row) { return (bf16_t*)(F.ws + WS_X) + (size_t)row * D; }
; __device__ __forceinline__ float wave_sum(float v) {
; #pragma unroll
;     for (int o = 1; o < 64; o <<= 1) v += __shfl_xor(v, o);
;     return v;
; }
; __device__ __forceinline__ void n1_finish16(Frame& F, int L, int row, const f32x4 (&v)[4], const f32x4 (&gs)[4], const f32x4 (&sh)[4]) {
;     { GAS u32x4* xo = (GAS u32x4*)x_row_ptr(F, row) + 2 * F.lane;
; #pragma unroll
;       for (int h = 0; h < 2; ++h) { u32x4 w; w.x = pk2(v[2 * h][0], v[2 * h][1]); w.y = pk2(v[2 * h][2], v[2 * h][3]); w.z = pk2(v[2 * h + 1][0], v[2 * h + 1][1]); w.w = pk2(v[2 * h + 1][2], v[2 * h + 1][3]); xo[h] = w; } }
;     float ss = 0.f;
; #pragma unroll
;     for (int j = 0; j < 4; ++j) ss += (v[j][0] * v[j][0] + v[j][1] * v[j][1]) + (v[j][2] * v[j][2] + v[j][3] * v[j][3]);
;     const float rinv = __builtin_amdgcn_rsqf(wave_sum(ss) * (1.0f / D) + EPS);
;     if ((L & 1) == 0) {
;         u32x4 o;
; #pragma unroll
;         for (int q = 0; q < 4; ++q) { const f32x4 h = ((v[q] * rinv) * gs[q] + sh[q]) * pg8::SC_H2; o[q] = pg8::pack4_fp8(h[0], h[1], h[2], h[3]); }
;         *((GAS u32x4*)((unsigned char*)(F.ws + WS_H) + (size_t)row * D) + F.lane) = o;
;     } else {
;         GAS u32x4* ho = (GAS u32x4*)((bf16_t*)(F.ws + WS_H) + (size_t)row * D) + 2 * F.lane;
; #pragma unroll
;         for (int hh = 0; hh < 2; ++hh) { const f32x4 h0 = (v[2 * hh] * rinv) * gs[2 * hh] + sh[2 * hh], h1 = (v[2 * hh + 1] * rinv) * gs[2 * hh + 1] + sh[2 * hh + 1];
;             u32x4 w; w.x = pk2(h0[0], h0[1]); w.y = pk2(h0[2], h0[3]); w.z = pk2(h1[0], h1[1]); w.w = pk2(h1[2], h1[3]); ho[hh] = w; }
.LBB0_334:
	s_ashr_i32 s5, s4, 31
	s_lshl_b64 s[2:3], s[4:5], 11
	v_readlane_b32 s0, v252, 20
	v_readlane_b32 s1, v252, 21
	s_add_u32 s0, s0, s2
	s_addc_u32 s1, s1, s3
	s_waitcnt vmcnt(10)
	v_cvt_pk_bf16_f32 v62, v118, v119
	v_cvt_pk_bf16_f32 v63, v120, v121
	v_cvt_pk_bf16_f32 v64, v114, v115
	v_cvt_pk_bf16_f32 v65, v116, v117
	s_nop 1
	global_store_dwordx4 v156, v[62:65], s[0:1]
	s_mov_b64 s[6:7], -1
	s_nop 0
	v_cvt_pk_bf16_f32 v62, v110, v111
	v_cvt_pk_bf16_f32 v63, v112, v113
	v_cvt_pk_bf16_f32 v64, v106, v107
	v_cvt_pk_bf16_f32 v65, v108, v109
	global_store_dwordx4 v156, v[62:65], s[0:1] offset:16
	v_readlane_b32 s0, v255, 17
	v_readlane_b32 s1, v255, 18
	v_mul_f32_e32 v62, v119, v119
	v_mul_f32_e32 v63, v121, v121
	v_fmac_f32_e32 v62, v118, v118
	v_fmac_f32_e32 v63, v120, v120
	v_add_f32_e32 v62, v62, v63
	v_mul_f32_e32 v63, v115, v115
	v_mul_f32_e32 v64, v117, v117
	v_fmac_f32_e32 v63, v114, v114
	v_fmac_f32_e32 v64, v116, v116
	v_add_f32_e32 v63, v63, v64
	v_add_f32_e32 v62, v63, v62
	v_mul_f32_e32 v63, v111, v111
	v_mul_f32_e32 v64, v113, v113
	v_fmac_f32_e32 v63, v110, v110
	v_fmac_f32_e32 v64, v112, v112
	v_add_f32_e32 v63, v63, v64
	v_add_f32_e32 v62, v63, v62
	v_mul_f32_e32 v63, v107, v107
	v_mul_f32_e32 v64, v109, v109
	v_fmac_f32_e32 v63, v106, v106
	v_fmac_f32_e32 v64, v108, v108
	v_add_f32_e32 v63, v63, v64
	v_add_f32_e32 v62, v63, v62
	v_and_b32_e32 v63, 64, v211
	v_add_u32_e32 v63, 64, v63
	v_xor_b32_e32 v64, 1, v211
	v_cmp_lt_i32_e32 vcc, v64, v63
	s_bitcmp1_b32 s0, 0
	s_cselect_b64 s[0:1], -1, 0
	v_cndmask_b32_e32 v64, v211, v64, vcc
	v_lshlrev_b32_e32 v84, 2, v64
	s_waitcnt lgkmcnt(0)
	s_nop 1
	v_mov_b32_dpp v64, v62 quad_perm:[1,0,3,2] row_mask:0xf bank_mask:0xf
	v_add_f32_e32 v62, v62, v64
	v_xor_b32_e32 v64, 2, v211
	v_cmp_lt_i32_e32 vcc, v64, v63
	s_nop 1
	v_cndmask_b32_e32 v64, v211, v64, vcc
	v_lshlrev_b32_e32 v85, 2, v64
	s_waitcnt lgkmcnt(0)
	s_nop 1
	v_mov_b32_dpp v64, v62 quad_perm:[2,3,0,1] row_mask:0xf bank_mask:0xf
	v_add_f32_e32 v62, v62, v64
	v_xor_b32_e32 v64, 4, v211
	v_cmp_lt_i32_e32 vcc, v64, v63
	s_nop 1
	v_cndmask_b32_e32 v64, v211, v64, vcc
	v_lshlrev_b32_e32 v86, 2, v64
	s_waitcnt lgkmcnt(0)
	s_nop 1
	v_mov_b32_dpp v64, v62 row_half_mirror row_mask:0xf bank_mask:0xf
	v_add_f32_e32 v62, v62, v64
	v_xor_b32_e32 v64, 8, v211
	v_cmp_lt_i32_e32 vcc, v64, v63
	s_nop 1
	v_cndmask_b32_e32 v64, v211, v64, vcc
	v_lshlrev_b32_e32 v87, 2, v64
	s_waitcnt lgkmcnt(0)
	s_nop 1
	v_mov_b32_dpp v64, v62 row_mirror row_mask:0xf bank_mask:0xf
	v_add_f32_e32 v62, v62, v64
	v_xor_b32_e32 v64, 16, v211
	v_cmp_lt_i32_e32 vcc, v64, v63
	s_nop 1
	v_cndmask_b32_e32 v64, v211, v64, vcc
	v_lshlrev_b32_e32 v88, 2, v64
	s_waitcnt lgkmcnt(0)
	v_mov_b32_e32 v64, v62
	s_nop 1
	v_permlane16_swap_b32_e32 v64, v62
	v_add_f32_e32 v62, v62, v64
	v_xor_b32_e32 v64, 32, v211
	v_cmp_lt_i32_e32 vcc, v64, v63
	s_nop 1
	v_cndmask_b32_e32 v63, v211, v64, vcc
	v_lshlrev_b32_e32 v89, 2, v63
	s_and_b64 vcc, exec, s[0:1]
	s_waitcnt lgkmcnt(0)
	v_mov_b32_e32 v63, v62
	s_nop 1
	v_permlane32_swap_b32_e32 v63, v62
	v_add_f32_e32 v62, v62, v63
	v_fmamk_f32 v62, v62, 0x3a800000, v250
	v_rsq_f32_e32 v62, v62
	s_cbranch_vccz .LBB0_336
	v_pk_mul_f32 v[78:79], v[62:63], v[118:119] op_sel_hi:[0,1]
	v_pk_mul_f32 v[80:81], v[62:63], v[116:117] op_sel_hi:[0,1]
	v_pk_mul_f32 v[82:83], v[62:63], v[114:115] op_sel_hi:[0,1]
	s_add_u32 s2, s96, s2
	v_pk_mul_f32 v[64:65], v[62:63], v[120:121] op_sel_hi:[0,1]
	v_pk_fma_f32 v[78:79], v[18:19], v[78:79], v[14:15]
	v_pk_fma_f32 v[90:91], v[24:25], v[80:81], v[12:13]
	v_pk_fma_f32 v[80:81], v[22:23], v[82:83], v[10:11]
	s_addc_u32 s3, s97, s3
	v_pk_fma_f32 v[64:65], v[20:21], v[64:65], v[16:17]
	v_cvt_pk_bf16_f32 v78, v78, v79
	v_cvt_pk_bf16_f32 v80, v80, v81
	v_cvt_pk_bf16_f32 v81, v90, v91
	v_pk_mul_f32 v[82:83], v[62:63], v[106:107] op_sel_hi:[0,1]
	v_cvt_pk_bf16_f32 v79, v64, v65
	global_store_dwordx4 v156, v[78:81], s[2:3]
	v_pk_mul_f32 v[64:65], v[62:63], v[112:113] op_sel_hi:[0,1]
	v_pk_fma_f32 v[64:65], v[28:29], v[64:65], v[8:9]
	v_pk_mul_f32 v[78:79], v[62:63], v[110:111] op_sel_hi:[0,1]
	v_pk_mul_f32 v[80:81], v[62:63], v[108:109] op_sel_hi:[0,1]
	v_pk_fma_f32 v[78:79], v[26:27], v[78:79], v[6:7]
	v_pk_fma_f32 v[90:91], v[32:33], v[80:81], v[4:5]
	v_pk_fma_f32 v[80:81], v[30:31], v[82:83], v[2:3]
	v_cvt_pk_bf16_f32 v78, v78, v79
	v_cvt_pk_bf16_f32 v79, v64, v65
	s_mov_b64 s[6:7], 0
	v_cvt_pk_bf16_f32 v80, v80, v81
	v_cvt_pk_bf16_f32 v81, v90, v91
	global_store_dwordx4 v156, v[78:81], s[2:3] offset:16

; #define GAS __attribute__((address_space(1)))
; __device__ __forceinline__ unsigned pk2(float lo, float hi) { unsigned r; asm("v_cvt_pk_bf16_f32 %0, %1, %2" : "=v"(r) : "v"(lo), "v"(hi)); return r; }
; __device__ __forceinline__ bf16_t* x_row_ptr(Frame& F, int row) { return (bf16_t*)(F.ws + WS_X) + (size_t)row * D; }
; __device__ __forceinline__ float wave_sum(float v) {
; #pragma unroll
;     for (int o = 1; o < 64; o <<= 1) v += __shfl_xor(v, o);
;     return v;
; }
; __device__ __forceinline__ void n1_finish16(Frame& F, int L, int row, const f32x4 (&v)[4], const f32x4 (&gs)[4], const f32x4 (&sh)[4]) {
;     { GAS u32x4* xo = (GAS u32x4*)x_row_ptr(F, row) + 2 * F.lane;
; #pragma unroll
;       for (int h = 0; h < 2; ++h) { u32x4 w; w.x = pk2(v[2 * h][0], v[2 * h][1]); w.y = pk2(v[2 * h][2], v[2 * h][3]); w.z = pk2(v[2 * h + 1][0], v[2 * h + 1][1]); w.w = pk2(v[2 * h + 1][2], v[2 * h + 1][3]); xo[h] = w; } }
;     float ss = 0.f;
; #pragma unroll
;     for (int j = 0; j < 4; ++j) ss += (v[j][0] * v[j][0] + v[j][1] * v[j][1]) + (v[j][2] * v[j][2] + v[j][3] * v[j][3]);
;     const float rinv = __builtin_amdgcn_rsqf(wave_sum(ss) * (1.0f / D) + EPS);
;     if ((L & 1) == 0) {
;         u32x4 o;
; #pragma unroll
;         for (int q = 0; q < 4; ++q) { const f32x4 h = ((v[q] * rinv) * gs[q] + sh[q]) * pg8::SC_H2; o[q] = pg8::pack4_fp8(h[0], h[1], h[2], h[3]); }
;         *((GAS u32x4*)((unsigned char*)(F.ws + WS_H) + (size_t)row * D) + F.lane) = o;
;     } else {
;         GAS u32x4* ho = (GAS u32x4*)((bf16_t*)(F.ws + WS_H) + (size_t)row * D) + 2 * F.lane;
; #pragma unroll
;         for (int hh = 0; hh < 2; ++hh) { const f32x4 h0 = (v[2 * hh] * rinv) * gs[2 * hh] + sh[2 * hh], h1 = (v[2 * hh + 1] * rinv) * gs[2 * hh + 1] + sh[2 * hh + 1];
;             u32x4 w; w.x = pk2(h0[0], h0[1]); w.y = pk2(h0[2], h0[3]); w.z = pk2(h1[0], h1[1]); w.w = pk2(h1[2], h1[3]); ho[hh] = w; }
.LBB0_360:
	s_waitcnt vmcnt(2)
	v_mul_f32_e32 v34, v81, v81
	v_mul_f32_e32 v35, v83, v83
	v_fmac_f32_e32 v34, v80, v80
	v_fmac_f32_e32 v35, v82, v82
	v_add_f32_e32 v34, v34, v35
	v_mul_f32_e32 v35, v79, v79
	v_mul_f32_e32 v36, v77, v77
	v_fmac_f32_e32 v35, v78, v78
	v_fmac_f32_e32 v36, v76, v76
	v_add_f32_e32 v35, v35, v36
	v_add_f32_e32 v34, v35, v34
	v_mul_f32_e32 v35, v75, v75
	v_mul_f32_e32 v36, v71, v71
	v_fmac_f32_e32 v35, v74, v74
	v_fmac_f32_e32 v36, v70, v70
	v_add_f32_e32 v35, v35, v36
	v_add_f32_e32 v34, v35, v34
	v_mul_f32_e32 v35, v63, v63
	v_mul_f32_e32 v36, v65, v65
	v_fmac_f32_e32 v35, v62, v62
	v_fmac_f32_e32 v36, v64, v64
	v_add_f32_e32 v35, v35, v36
	v_add_f32_e32 v34, v35, v34
	s_ashr_i32 s5, s4, 31
	s_lshl_b64 s[2:3], s[4:5], 11
	v_readlane_b32 s6, v252, 20
	v_readlane_b32 s7, v252, 21
	s_waitcnt lgkmcnt(0)
	s_nop 1
	v_mov_b32_dpp v35, v34 quad_perm:[1,0,3,2] row_mask:0xf bank_mask:0xf
	v_add_f32_e32 v34, v34, v35
	s_add_u32 s6, s6, s2
	s_addc_u32 s7, s7, s3
	s_and_b64 vcc, exec, s[0:1]
	s_waitcnt lgkmcnt(0)
	s_nop 1
	v_mov_b32_dpp v35, v34 quad_perm:[2,3,0,1] row_mask:0xf bank_mask:0xf
	v_add_f32_e32 v34, v34, v35
	s_waitcnt lgkmcnt(0)
	s_nop 1
	v_mov_b32_dpp v35, v34 row_half_mirror row_mask:0xf bank_mask:0xf
	v_add_f32_e32 v36, v34, v35
	v_cvt_pk_bf16_f32 v34, v80, v81
	v_cvt_pk_bf16_f32 v35, v82, v83
	s_waitcnt lgkmcnt(0)
	s_nop 1
	v_mov_b32_dpp v37, v36 row_mirror row_mask:0xf bank_mask:0xf
	v_add_f32_e32 v38, v36, v37
	v_cvt_pk_bf16_f32 v36, v78, v79
	v_cvt_pk_bf16_f32 v37, v76, v77
	global_store_dwordx4 v156, v[34:37], s[6:7]
	s_waitcnt lgkmcnt(0)
	v_mov_b32_e32 v39, v38
	s_nop 1
	v_permlane16_swap_b32_e32 v39, v38
	v_add_f32_e32 v38, v38, v39
	v_cvt_pk_bf16_f32 v34, v74, v75
	v_cvt_pk_bf16_f32 v35, v70, v71
	v_cvt_pk_bf16_f32 v36, v62, v63
	v_cvt_pk_bf16_f32 v37, v64, v65
	global_store_dwordx4 v156, v[34:37], s[6:7] offset:16
	s_mov_b64 s[6:7], -1
	s_waitcnt lgkmcnt(0)
	v_mov_b32_e32 v39, v38
	v_mov_b32_e32 v34, v38
	s_nop 1
	v_permlane32_swap_b32_e32 v39, v34
	v_add_f32_e32 v34, v34, v39
	v_fmamk_f32 v34, v34, 0x3a800000, v250
	v_rsq_f32_e32 v34, v34
	s_cbranch_vccz .LBB0_362
	v_pk_mul_f32 v[36:37], v[34:35], v[82:83] op_sel_hi:[0,1]
	v_pk_mul_f32 v[38:39], v[34:35], v[80:81] op_sel_hi:[0,1]
	v_pk_fma_f32 v[40:41], v[20:21], v[36:37], v[16:17]
	v_pk_fma_f32 v[36:37], v[18:19], v[38:39], v[14:15]
	v_pk_mul_f32 v[38:39], v[34:35], v[76:77] op_sel_hi:[0,1]
	v_pk_mul_f32 v[42:43], v[34:35], v[78:79] op_sel_hi:[0,1]
	s_add_u32 s0, s96, s2
	v_pk_fma_f32 v[44:45], v[24:25], v[38:39], v[12:13]
	v_pk_fma_f32 v[38:39], v[22:23], v[42:43], v[10:11]
	s_addc_u32 s1, s97, s3
	v_cvt_pk_bf16_f32 v36, v36, v37
	v_cvt_pk_bf16_f32 v37, v40, v41
	v_cvt_pk_bf16_f32 v38, v38, v39
	v_cvt_pk_bf16_f32 v39, v44, v45
	global_store_dwordx4 v156, v[36:39], s[0:1]
	v_pk_mul_f32 v[42:43], v[34:35], v[62:63] op_sel_hi:[0,1]
	s_mov_b64 s[6:7], 0
	v_pk_mul_f32 v[36:37], v[34:35], v[70:71] op_sel_hi:[0,1]
	v_pk_mul_f32 v[38:39], v[34:35], v[74:75] op_sel_hi:[0,1]
	v_pk_fma_f32 v[40:41], v[28:29], v[36:37], v[8:9]
	v_pk_fma_f32 v[36:37], v[26:27], v[38:39], v[6:7]
	v_pk_mul_f32 v[38:39], v[34:35], v[64:65] op_sel_hi:[0,1]
	v_pk_fma_f32 v[44:45], v[32:33], v[38:39], v[4:5]
	v_pk_fma_f32 v[38:39], v[30:31], v[42:43], v[2:3]
	v_cvt_pk_bf16_f32 v36, v36, v37
	v_cvt_pk_bf16_f32 v37, v40, v41
	s_nop 0
	v_cvt_pk_bf16_f32 v38, v38, v39
	v_cvt_pk_bf16_f32 v39, v44, v45
	global_store_dwordx4 v156, v[36:39], s[0:1] offset:16

; #define GAS __attribute__((address_space(1)))
; __device__ __forceinline__ unsigned pk2(float lo, float hi) { unsigned r; asm("v_cvt_pk_bf16_f32 %0, %1, %2" : "=v"(r) : "v"(lo), "v"(hi)); return r; }
; __device__ __forceinline__ bf16_t* x_row_ptr(Frame& F, int row) { return (bf16_t*)(F.ws + WS_X) + (size_t)row * D; }
; #define N1_XLD(X, r) do { const GAS f32x4* xin_ = (const GAS f32x4*)N1_XIN(r) + F.lane; _Pragma("unroll") for (int j = 0; j < 4; ++j) X[j] = xin_[64 * j]; } while (0)
; #define N1_STEP0(XC, XI, kk) do { const int k_ = (kk), row_ = rbeg + k_; N1_MOD(row_); N1_XLD(XI, rbeg + (k_ + 2 < RPW ? k_ + 2 : RPW - 1)); n1_finish(F, L, row_, XC, gs, sh); } while (0)
; __device__ __forceinline__ void n1_finish(Frame& F, int L, int row, const f32x4 (&v)[4], const f32x4 (&gs)[4], const f32x4 (&sh)[4]) {
;     bf16_t* H = (bf16_t*)(F.ws + WS_H);
;     x_store_row(x_row_ptr(F, row), F.lane, v);
;     float ss = 0.f;
; #pragma unroll
;     for (int j = 0; j < 4; ++j) ss += (v[j][0] * v[j][0] + v[j][1] * v[j][1]) + (v[j][2] * v[j][2] + v[j][3] * v[j][3]);
;     const float rinv = __builtin_amdgcn_rsqf(wave_sum(ss) * (1.0f / D) + EPS);
;     if ((L & 1) == 0) {
;         GAS unsigned* o4 = (GAS unsigned*)((unsigned char*)H + (size_t)row * D) + F.lane;
; #pragma unroll
;         for (int j = 0; j < 4; ++j) { const f32x4 h = ((v[j] * rinv) * gs[j] + sh[j]) * pg8::SC_H2; o4[64 * j] = pg8::pack4_fp8(h[0], h[1], h[2], h[3]); }
;     } else {
;         GAS u32x2* o8 = (GAS u32x2*)(H + (size_t)row * D) + F.lane;
; #pragma unroll
;         for (int j = 0; j < 4; ++j) { const f32x4 h = (v[j] * rinv) * gs[j] + sh[j]; u32x2 w; w.x = pk2(h[0], h[1]); w.y = pk2(h[2], h[3]); o8[64 * j] = w; }
;     }
; }
; __device__ __forceinline__ void n1_phase(const Frame& F0, int L, int nrows) {
;     ...
;         f32x4 X0[4], X1[4], X2[4];
;         N1_XLD(X0, rbeg); N1_XLD(X1, rbeg + 1);
;         int k = 0;
;         for (; k + 2 < RPW; k += 3) { N1_STEP0(X0, X2, k); N1_STEP0(X1, X0, k + 1); N1_STEP0(X2, X1, k + 2); }
.LBB0_381:
	s_waitcnt vmcnt(7)
	v_pk_mul_f32 v[66:67], v[64:65], v[64:65]
	v_pk_mul_f32 v[68:69], v[62:63], v[62:63]
	s_lshl_b64 s[4:5], s[4:5], 12
	v_pk_mov_b32 v[70:71], v[68:69], v[66:67] op_sel:[1,0]
	v_mov_b32_e32 v69, v67
	v_pk_add_f32 v[66:67], v[70:71], v[68:69]
	s_waitcnt vmcnt(6)
	v_pk_mul_f32 v[68:69], v[60:61], v[60:61]
	v_pk_add_f32 v[66:67], v[66:67], v[66:67] op_sel_hi:[0,1]
	v_pk_mul_f32 v[70:71], v[58:59], v[58:59]
	s_waitcnt vmcnt(5)
	v_mul_f32_e32 v66, v54, v54
	v_pk_mov_b32 v[72:73], v[70:71], v[68:69] op_sel:[1,0]
	v_mov_b32_e32 v71, v69
	v_pk_add_f32 v[68:69], v[72:73], v[70:71]
	v_pk_fma_f32 v[70:71], v[54:55], v[54:55], v[66:67] op_sel_hi:[1,1,0]
	v_mul_f32_e32 v66, v56, v56
	v_pk_add_f32 v[68:69], v[68:69], v[68:69] op_sel_hi:[0,1]
	v_pk_fma_f32 v[72:73], v[56:57], v[56:57], v[66:67] op_sel_hi:[1,1,0]
	s_waitcnt vmcnt(4)
	v_mul_f32_e32 v70, v46, v46
	v_mul_f32_e32 v72, v47, v47
	v_mul_f32_e32 v68, v48, v48
	v_mul_f32_e32 v66, v49, v49
	v_pk_add_f32 v[70:71], v[70:71], v[72:73]
	v_pk_add_f32 v[66:67], v[68:69], v[66:67]
	s_add_u32 s2, s2, s4
	v_pk_add_f32 v[66:67], v[70:71], v[66:67]
	s_addc_u32 s3, s3, s5
	v_add_f32_e32 v66, v66, v67
	v_and_b32_e32 v67, 64, v211
	v_add_u32_e32 v110, 64, v67
	v_xor_b32_e32 v67, 1, v211
	v_cmp_lt_i32_e32 vcc, v67, v110
	global_load_dwordx4 v[78:81], v84, s[2:3] nt
	global_load_dwordx4 v[74:77], v84, s[2:3] offset:1024 nt
	v_cndmask_b32_e32 v67, v211, v67, vcc
	v_lshlrev_b32_e32 v91, 2, v67
	v_lshl_add_u64 v[104:105], s[82:83], 0, v[100:101]
	s_mov_b32 s1, 0x31b00000
	v_cvt_pk_bf16_f32 v107, v64, v65
	v_cvt_pk_bf16_f32 v106, v62, v63
	s_waitcnt lgkmcnt(0)
	s_nop 1
	v_mov_b32_dpp v67, v66 quad_perm:[1,0,3,2] row_mask:0xf bank_mask:0xf
	v_add_f32_e32 v66, v66, v67
	v_xor_b32_e32 v67, 2, v211
	v_cmp_lt_i32_e32 vcc, v67, v110
	s_nop 1
	v_cndmask_b32_e32 v67, v211, v67, vcc
	v_lshlrev_b32_e32 v93, 2, v67
	s_waitcnt lgkmcnt(0)
	s_nop 1
	v_mov_b32_dpp v67, v66 quad_perm:[2,3,0,1] row_mask:0xf bank_mask:0xf
	v_add_f32_e32 v103, v66, v67
	v_xor_b32_e32 v66, 4, v211
	v_cmp_lt_i32_e32 vcc, v66, v110
	s_nop 1
	v_cndmask_b32_e32 v66, v211, v66, vcc
	v_lshlrev_b32_e32 v102, 2, v66
	global_load_dwordx4 v[70:73], v84, s[2:3] offset:2048 nt
	global_load_dwordx4 v[66:69], v84, s[2:3] offset:3072 nt
	s_add_i32 s2, s8, -3
	s_waitcnt lgkmcnt(0)
	s_nop 1
	v_mov_b32_dpp v108, v103 row_half_mirror row_mask:0xf bank_mask:0xf
	v_add_f32_e32 v111, v103, v108
	v_xor_b32_e32 v103, 8, v211
	v_cmp_lt_i32_e32 vcc, v103, v110
	s_nop 1
	v_cndmask_b32_e32 v103, v211, v103, vcc
	v_lshlrev_b32_e32 v103, 2, v103
	v_add_co_u32_e32 v108, vcc, s1, v104
	v_xor_b32_e32 v104, 16, v211
	s_nop 0
	v_addc_co_u32_e32 v109, vcc, 0, v105, vcc
	v_cmp_lt_i32_e32 vcc, v104, v110
	s_waitcnt lgkmcnt(0)
	s_nop 1
	v_mov_b32_dpp v112, v111 row_mirror row_mask:0xf bank_mask:0xf
	v_add_f32_e32 v105, v111, v112
	global_store_dwordx2 v[108:109], v[106:107], off
	v_cndmask_b32_e32 v104, v211, v104, vcc
	v_lshlrev_b32_e32 v104, 2, v104
	v_cvt_pk_bf16_f32 v107, v60, v61
	v_cvt_pk_bf16_f32 v106, v58, v59
	global_store_dwordx2 v[108:109], v[106:107], off offset:512
	v_cvt_pk_bf16_f32 v107, v56, v57
	s_waitcnt lgkmcnt(0)
	v_mov_b32_e32 v111, v105
	s_nop 1
	v_permlane16_swap_b32_e32 v111, v105
	v_add_f32_e32 v111, v105, v111
	v_xor_b32_e32 v105, 32, v211
	v_cmp_lt_i32_e32 vcc, v105, v110
	v_cvt_pk_bf16_f32 v106, v54, v55
	global_store_dwordx2 v[108:109], v[106:107], off offset:1024
	v_cvt_pk_bf16_f32 v106, v46, v47
	s_mov_b32 s1, 0x1b300000
	v_cndmask_b32_e32 v105, v211, v105, vcc
	v_lshlrev_b32_e32 v105, 2, v105
	s_waitcnt lgkmcnt(0)
	v_mov_b32_e32 v110, v111
	v_mov_b32_e32 v107, v111
	s_nop 1
	v_permlane32_swap_b32_e32 v110, v107
	v_add_f32_e32 v107, v107, v110
	v_fmamk_f32 v107, v107, 0x3a800000, v250
	v_rsq_f32_e32 v110, v107
	v_cvt_pk_bf16_f32 v107, v48, v49
	global_store_dwordx2 v[108:109], v[106:107], off offset:1536
	v_mov_b32_e32 v108, v191
	v_pk_mul_f32 v[62:63], v[62:63], v[110:111] op_sel_hi:[1,0]
	v_pk_mul_f32 v[64:65], v[64:65], v[110:111] op_sel_hi:[1,0]
	v_pk_fma_f32 v[62:63], v[50:51], v[62:63], v[26:27]
	v_pk_fma_f32 v[64:65], v[52:53], v[64:65], v[28:29]
	v_pk_mul_f32 v[62:63], v[62:63], s[16:17] op_sel_hi:[1,0]
	v_pk_mul_f32 v[58:59], v[58:59], v[110:111] op_sel_hi:[1,0]
	v_med3_f32 v62, v62, s15, v212
	v_med3_f32 v63, v63, s15, v212
	v_cvt_pk_fp8_f32 v108, v62, v63
	v_pk_mul_f32 v[62:63], v[64:65], s[16:17] op_sel_hi:[1,0]
	v_pk_fma_f32 v[58:59], v[42:43], v[58:59], v[22:23]
	v_med3_f32 v62, v62, s15, v212
	v_med3_f32 v63, v63, s15, v212
	v_pk_mul_f32 v[58:59], v[58:59], s[16:17] op_sel_hi:[1,0]
	v_cvt_pk_fp8_f32 v108, v62, v63 op_sel:[0,0,1]
	v_med3_f32 v58, v58, s15, v212
	v_med3_f32 v59, v59, s15, v212
	v_mov_b32_e32 v62, v191
	v_pk_mul_f32 v[60:61], v[60:61], v[110:111] op_sel_hi:[1,0]
	v_cvt_pk_fp8_f32 v62, v58, v59
	v_pk_fma_f32 v[60:61], v[44:45], v[60:61], v[24:25]
	v_pk_mul_f32 v[54:55], v[54:55], v[110:111] op_sel_hi:[1,0]
	v_pk_mul_f32 v[58:59], v[60:61], s[16:17] op_sel_hi:[1,0]
	v_pk_fma_f32 v[54:55], v[38:39], v[54:55], v[18:19]
	v_pk_mul_f32 v[46:47], v[46:47], v[110:111] op_sel_hi:[1,0]
	v_med3_f32 v58, v58, s15, v212
	v_med3_f32 v59, v59, s15, v212
	v_pk_mul_f32 v[56:57], v[56:57], v[110:111] op_sel_hi:[1,0]
	v_pk_mul_f32 v[54:55], v[54:55], s[16:17] op_sel_hi:[1,0]
	v_pk_fma_f32 v[46:47], v[34:35], v[46:47], v[30:31]
	v_cvt_pk_fp8_f32 v62, v58, v59 op_sel:[0,0,1]
	v_pk_fma_f32 v[56:57], v[40:41], v[56:57], v[20:21]
	v_med3_f32 v54, v54, s15, v212
	v_med3_f32 v55, v55, s15, v212
	v_mov_b32_e32 v58, v191
	v_pk_mul_f32 v[46:47], v[46:47], s[16:17] op_sel_hi:[1,0]
	v_cvt_pk_fp8_f32 v58, v54, v55
	v_pk_mul_f32 v[54:55], v[56:57], s[16:17] op_sel_hi:[1,0]
	v_med3_f32 v46, v46, s15, v212
	v_med3_f32 v47, v47, s15, v212
	v_mov_b32_e32 v56, v191
	v_pk_mul_f32 v[48:49], v[48:49], v[110:111] op_sel_hi:[1,0]
	v_cvt_pk_fp8_f32 v56, v46, v47
	v_pk_fma_f32 v[48:49], v[36:37], v[48:49], v[32:33]
	v_lshl_add_u64 v[106:107], s[82:83], 0, v[98:99]
	v_pk_mul_f32 v[46:47], v[48:49], s[16:17] op_sel_hi:[1,0]
	v_med3_f32 v54, v54, s15, v212
	v_med3_f32 v46, v46, s15, v212
	v_med3_f32 v47, v47, s15, v212
	v_med3_f32 v55, v55, s15, v212
	v_cvt_pk_fp8_f32 v56, v46, v47 op_sel:[0,0,1]
	v_cvt_pk_fp8_f32 v58, v54, v55 op_sel:[0,0,1]
	v_add_co_u32_e32 v54, vcc, s1, v106
	s_min_i32 s1, s2, 0x8000
	s_ashr_i32 s1, s1, 11
	v_addc_co_u32_e32 v55, vcc, 0, v107, vcc
	s_cmp_eq_u32 s1, s17
	global_store_dword v[54:55], v108, off
	global_store_dword v[54:55], v62, off offset:256
	global_store_dword v[54:55], v58, off offset:512
	global_store_dword v[54:55], v56, off offset:768
	s_cbranch_scc1 .LBB0_383
	s_mul_i32 s4, s1, 0x1800
	s_ashr_i32 s5, s4, 31
	s_lshl_b64 s[4:5], s[4:5], 2
	v_readlane_b32 s3, v255, 20
	s_add_u32 s4, s3, s4
	v_readlane_b32 s3, v255, 21
	s_addc_u32 s5, s3, s5
	s_add_u32 s6, s4, 0x1000
	s_addc_u32 s7, s5, 0
	global_load_dwordx4 v[34:37], v1, s[6:7]
	global_load_dwordx4 v[38:41], v89, s[6:7]
	global_load_dwordx4 v[42:45], v85, s[6:7]
	global_load_dwordx4 v[46:49], v83, s[6:7]
	flat_load_dwordx4 v[50:53], v[86:87]
	flat_load_dwordx4 v[54:57], v[86:87] offset:1024
	flat_load_dwordx4 v[58:61], v[86:87] offset:2048
	flat_load_dwordx4 v[62:65], v[86:87] offset:3072
	global_load_dwordx4 v[26:29], v1, s[4:5] nt
	global_load_dwordx4 v[22:25], v1, s[4:5] offset:1024 nt
	global_load_dwordx4 v[18:21], v1, s[4:5] offset:2048 nt
	global_load_dwordx4 v[30:33], v1, s[4:5] offset:3072 nt
	s_mov_b32 s17, s1
	s_waitcnt vmcnt(0)
	v_pk_add_f32 v[36:37], v[36:37], 1.0 op_sel_hi:[1,0]
	v_pk_add_f32 v[34:35], v[34:35], 1.0 op_sel_hi:[1,0]
	v_pk_add_f32 v[40:41], v[40:41], 1.0 op_sel_hi:[1,0]
	v_pk_add_f32 v[38:39], v[38:39], 1.0 op_sel_hi:[1,0]
	v_pk_add_f32 v[106:107], v[44:45], 1.0 op_sel_hi:[1,0]
	v_pk_add_f32 v[108:109], v[42:43], 1.0 op_sel_hi:[1,0]
	v_pk_add_f32 v[48:49], v[48:49], 1.0 op_sel_hi:[1,0]
	v_pk_add_f32 v[46:47], v[46:47], 1.0 op_sel_hi:[1,0]
	s_waitcnt lgkmcnt(0)
	v_pk_mul_f32 v[52:53], v[52:53], v[36:37]
	v_pk_mul_f32 v[50:51], v[50:51], v[34:35]
	v_pk_mul_f32 v[44:45], v[56:57], v[40:41]
	v_pk_mul_f32 v[42:43], v[54:55], v[38:39]
	v_pk_mul_f32 v[40:41], v[60:61], v[106:107]
	v_pk_mul_f32 v[38:39], v[58:59], v[108:109]
	v_pk_mul_f32 v[36:37], v[64:65], v[48:49]
	v_pk_mul_f32 v[34:35], v[62:63], v[46:47]

; #define GAS __attribute__((address_space(1)))
; __device__ __forceinline__ unsigned pk2(float lo, float hi) { unsigned r; asm("v_cvt_pk_bf16_f32 %0, %1, %2" : "=v"(r) : "v"(lo), "v"(hi)); return r; }
; __device__ __forceinline__ bf16_t* x_row_ptr(Frame& F, int row) { return (bf16_t*)(F.ws + WS_X) + (size_t)row * D; }
; __device__ __forceinline__ void n1_finish(Frame& F, int L, int row, const f32x4 (&v)[4], const f32x4 (&gs)[4], const f32x4 (&sh)[4]) {
;     bf16_t* H = (bf16_t*)(F.ws + WS_H);
;     x_store_row(x_row_ptr(F, row), F.lane, v);
;     float ss = 0.f;
; #pragma unroll
;     for (int j = 0; j < 4; ++j) ss += (v[j][0] * v[j][0] + v[j][1] * v[j][1]) + (v[j][2] * v[j][2] + v[j][3] * v[j][3]);
;     const float rinv = __builtin_amdgcn_rsqf(wave_sum(ss) * (1.0f / D) + EPS);
;     if ((L & 1) == 0) {
;         GAS unsigned* o4 = (GAS unsigned*)((unsigned char*)H + (size_t)row * D) + F.lane;
; #pragma unroll
;         for (int j = 0; j < 4; ++j) { const f32x4 h = ((v[j] * rinv) * gs[j] + sh[j]) * pg8::SC_H2; o4[64 * j] = pg8::pack4_fp8(h[0], h[1], h[2], h[3]); }
;     } else {
;         GAS u32x2* o8 = (GAS u32x2*)(H + (size_t)row * D) + F.lane;
; #pragma unroll
;         for (int j = 0; j < 4; ++j) { const f32x4 h = (v[j] * rinv) * gs[j] + sh[j]; u32x2 w; w.x = pk2(h[0], h[1]); w.y = pk2(h[2], h[3]); o8[64 * j] = w; }
;     }
; }
.LBB0_387:
	s_waitcnt vmcnt(15)
	v_pk_mul_f32 v[46:47], v[16:17], v[16:17]
	v_pk_mul_f32 v[48:49], v[14:15], v[14:15]
	s_lshl_b64 s[6:7], s[6:7], 12
	v_pk_mov_b32 v[54:55], v[48:49], v[46:47] op_sel:[1,0]
	v_mov_b32_e32 v49, v47
	v_pk_add_f32 v[46:47], v[54:55], v[48:49]
	s_waitcnt vmcnt(14)
	v_pk_mul_f32 v[48:49], v[12:13], v[12:13]
	v_pk_add_f32 v[46:47], v[46:47], v[46:47] op_sel_hi:[0,1]
	v_pk_mul_f32 v[54:55], v[10:11], v[10:11]
	s_waitcnt vmcnt(13)
	v_mul_f32_e32 v46, v6, v6
	v_pk_mov_b32 v[56:57], v[54:55], v[48:49] op_sel:[1,0]
	v_mov_b32_e32 v55, v49
	v_pk_add_f32 v[48:49], v[56:57], v[54:55]
	v_pk_fma_f32 v[54:55], v[6:7], v[6:7], v[46:47] op_sel_hi:[1,1,0]
	v_mul_f32_e32 v46, v8, v8
	v_pk_add_f32 v[48:49], v[48:49], v[48:49] op_sel_hi:[0,1]
	v_pk_fma_f32 v[56:57], v[8:9], v[8:9], v[46:47] op_sel_hi:[1,1,0]
	s_waitcnt vmcnt(12)
	v_mul_f32_e32 v54, v2, v2
	v_mul_f32_e32 v56, v3, v3
	v_mul_f32_e32 v48, v4, v4
	v_mul_f32_e32 v46, v5, v5
	v_pk_add_f32 v[54:55], v[54:55], v[56:57]
	v_pk_add_f32 v[46:47], v[48:49], v[46:47]
	s_add_u32 s4, s4, s6
	v_pk_add_f32 v[46:47], v[54:55], v[46:47]
	s_addc_u32 s5, s5, s7
	v_add_f32_e32 v46, v46, v47
	s_ashr_i32 s3, s2, 31
	s_min_i32 s1, s0, 0x8000
	s_ashr_i32 s1, s1, 11
	s_waitcnt lgkmcnt(0)
	s_nop 1
	v_mov_b32_dpp v47, v46 quad_perm:[1,0,3,2] row_mask:0xf bank_mask:0xf
	v_add_f32_e32 v46, v46, v47
	s_waitcnt lgkmcnt(0)
	s_nop 1
	v_mov_b32_dpp v47, v46 quad_perm:[2,3,0,1] row_mask:0xf bank_mask:0xf
	v_add_f32_e32 v106, v46, v47
	global_load_dwordx4 v[62:65], v84, s[4:5] nt
	global_load_dwordx4 v[58:61], v84, s[4:5] offset:1024 nt
	global_load_dwordx4 v[54:57], v84, s[4:5] offset:2048 nt
	global_load_dwordx4 v[46:49], v84, s[4:5] offset:3072 nt
	s_lshl_b64 s[4:5], s[2:3], 11
	v_lshl_add_u64 v[108:109], v[94:95], 0, s[4:5]
	s_lshl_b64 s[2:3], s[2:3], 10
	s_cmp_eq_u32 s1, s17
	s_waitcnt lgkmcnt(0)
	s_nop 1
	v_mov_b32_dpp v107, v106 row_half_mirror row_mask:0xf bank_mask:0xf
	v_add_f32_e32 v110, v106, v107
	v_cvt_pk_bf16_f32 v107, v16, v17
	v_cvt_pk_bf16_f32 v106, v14, v15
	global_store_dwordx2 v[108:109], v[106:107], off
	v_cvt_pk_bf16_f32 v107, v12, v13
	s_waitcnt lgkmcnt(0)
	s_nop 1
	v_mov_b32_dpp v111, v110 row_mirror row_mask:0xf bank_mask:0xf
	v_add_f32_e32 v110, v110, v111
	v_cvt_pk_bf16_f32 v106, v10, v11
	global_store_dwordx2 v[108:109], v[106:107], off offset:512
	v_cvt_pk_bf16_f32 v107, v8, v9
	v_cvt_pk_bf16_f32 v106, v6, v7
	s_waitcnt lgkmcnt(0)
	v_mov_b32_e32 v111, v110
	s_nop 1
	v_permlane16_swap_b32_e32 v111, v110
	v_add_f32_e32 v110, v110, v111
	global_store_dwordx2 v[108:109], v[106:107], off offset:1024
	v_cvt_pk_bf16_f32 v106, v2, v3
	s_waitcnt lgkmcnt(0)
	v_mov_b32_e32 v111, v110
	v_mov_b32_e32 v107, v110
	s_nop 1
	v_permlane32_swap_b32_e32 v111, v107
	v_add_f32_e32 v107, v107, v111
	v_fmamk_f32 v107, v107, 0x3a800000, v250
	v_rsq_f32_e32 v110, v107
	v_cvt_pk_bf16_f32 v107, v4, v5
	global_store_dwordx2 v[108:109], v[106:107], off offset:1536
	v_mov_b32_e32 v106, v191
	v_pk_mul_f32 v[14:15], v[14:15], v[110:111] op_sel_hi:[1,0]
	v_pk_mul_f32 v[16:17], v[16:17], v[110:111] op_sel_hi:[1,0]
	v_pk_fma_f32 v[14:15], v[50:51], v[14:15], v[26:27]
	v_pk_fma_f32 v[16:17], v[52:53], v[16:17], v[28:29]
	v_pk_mul_f32 v[14:15], v[14:15], s[16:17] op_sel_hi:[1,0]
	v_pk_mul_f32 v[10:11], v[10:11], v[110:111] op_sel_hi:[1,0]
	v_med3_f32 v14, v14, s15, v212
	v_med3_f32 v15, v15, s15, v212
	v_cvt_pk_fp8_f32 v106, v14, v15
	v_pk_mul_f32 v[14:15], v[16:17], s[16:17] op_sel_hi:[1,0]
	v_pk_fma_f32 v[10:11], v[42:43], v[10:11], v[22:23]
	v_med3_f32 v14, v14, s15, v212
	v_med3_f32 v15, v15, s15, v212
	v_pk_mul_f32 v[10:11], v[10:11], s[16:17] op_sel_hi:[1,0]
	v_cvt_pk_fp8_f32 v106, v14, v15 op_sel:[0,0,1]
	v_med3_f32 v10, v10, s15, v212
	v_med3_f32 v11, v11, s15, v212
	v_mov_b32_e32 v14, v191
	v_pk_mul_f32 v[12:13], v[12:13], v[110:111] op_sel_hi:[1,0]
	v_cvt_pk_fp8_f32 v14, v10, v11
	v_pk_fma_f32 v[12:13], v[44:45], v[12:13], v[24:25]
	v_pk_mul_f32 v[6:7], v[6:7], v[110:111] op_sel_hi:[1,0]
	v_pk_mul_f32 v[10:11], v[12:13], s[16:17] op_sel_hi:[1,0]
	v_pk_fma_f32 v[6:7], v[38:39], v[6:7], v[18:19]
	v_pk_mul_f32 v[2:3], v[2:3], v[110:111] op_sel_hi:[1,0]
	v_med3_f32 v10, v10, s15, v212
	v_med3_f32 v11, v11, s15, v212
	v_pk_mul_f32 v[8:9], v[8:9], v[110:111] op_sel_hi:[1,0]
	v_pk_mul_f32 v[6:7], v[6:7], s[16:17] op_sel_hi:[1,0]
	v_pk_fma_f32 v[2:3], v[34:35], v[2:3], v[30:31]
	v_cvt_pk_fp8_f32 v14, v10, v11 op_sel:[0,0,1]
	v_pk_fma_f32 v[8:9], v[40:41], v[8:9], v[20:21]
	v_med3_f32 v6, v6, s15, v212
	v_med3_f32 v7, v7, s15, v212
	v_mov_b32_e32 v10, v191
	v_pk_mul_f32 v[2:3], v[2:3], s[16:17] op_sel_hi:[1,0]
	v_cvt_pk_fp8_f32 v10, v6, v7
	v_pk_mul_f32 v[6:7], v[8:9], s[16:17] op_sel_hi:[1,0]
	v_med3_f32 v2, v2, s15, v212
	v_med3_f32 v3, v3, s15, v212
	v_mov_b32_e32 v8, v191
	v_pk_mul_f32 v[4:5], v[4:5], v[110:111] op_sel_hi:[1,0]
	v_cvt_pk_fp8_f32 v8, v2, v3
	v_pk_fma_f32 v[4:5], v[36:37], v[4:5], v[32:33]
	v_med3_f32 v6, v6, s15, v212
	v_pk_mul_f32 v[2:3], v[4:5], s[16:17] op_sel_hi:[1,0]
	v_med3_f32 v7, v7, s15, v212
	v_med3_f32 v2, v2, s15, v212
	v_med3_f32 v3, v3, s15, v212
	v_cvt_pk_fp8_f32 v8, v2, v3 op_sel:[0,0,1]
	v_cvt_pk_fp8_f32 v10, v6, v7 op_sel:[0,0,1]
	v_lshl_add_u64 v[6:7], v[96:97], 0, s[2:3]
	global_store_dword v[6:7], v106, off
	global_store_dword v[6:7], v14, off offset:256
	global_store_dword v[6:7], v10, off offset:512
	global_store_dword v[6:7], v8, off offset:768
	s_cbranch_scc1 .LBB0_389
	s_mul_i32 s2, s1, 0x1800
	s_ashr_i32 s3, s2, 31
	s_lshl_b64 s[2:3], s[2:3], 2
	v_readlane_b32 s4, v255, 20
	s_add_u32 s2, s4, s2
	v_readlane_b32 s4, v255, 21
	s_addc_u32 s3, s4, s3
	s_add_u32 s4, s2, 0x1000
	s_addc_u32 s5, s3, 0
	s_nop 1
	global_load_dwordx4 v[2:5], v1, s[4:5]
	global_load_dwordx4 v[6:9], v89, s[4:5]
	global_load_dwordx4 v[10:13], v85, s[4:5]
	global_load_dwordx4 v[14:17], v83, s[4:5]
	flat_load_dwordx4 v[34:37], v[86:87]
	flat_load_dwordx4 v[38:41], v[86:87] offset:1024
	flat_load_dwordx4 v[106:109], v[86:87] offset:2048
	flat_load_dwordx4 v[110:113], v[86:87] offset:3072
	global_load_dwordx4 v[26:29], v1, s[2:3] nt
	global_load_dwordx4 v[22:25], v1, s[2:3] offset:1024 nt
	global_load_dwordx4 v[18:21], v1, s[2:3] offset:2048 nt
	global_load_dwordx4 v[30:33], v1, s[2:3] offset:3072 nt
	s_mov_b32 s17, s1
	s_waitcnt vmcnt(0)
	v_pk_add_f32 v[4:5], v[4:5], 1.0 op_sel_hi:[1,0]
	v_pk_add_f32 v[2:3], v[2:3], 1.0 op_sel_hi:[1,0]
	v_pk_add_f32 v[8:9], v[8:9], 1.0 op_sel_hi:[1,0]
	v_pk_add_f32 v[6:7], v[6:7], 1.0 op_sel_hi:[1,0]
	v_pk_add_f32 v[12:13], v[12:13], 1.0 op_sel_hi:[1,0]
	v_pk_add_f32 v[10:11], v[10:11], 1.0 op_sel_hi:[1,0]
	v_pk_add_f32 v[16:17], v[16:17], 1.0 op_sel_hi:[1,0]
	v_pk_add_f32 v[14:15], v[14:15], 1.0 op_sel_hi:[1,0]
	s_waitcnt lgkmcnt(0)
	v_pk_mul_f32 v[52:53], v[36:37], v[4:5]
	v_pk_mul_f32 v[50:51], v[34:35], v[2:3]
	v_pk_mul_f32 v[44:45], v[40:41], v[8:9]
	v_pk_mul_f32 v[42:43], v[38:39], v[6:7]
	v_pk_mul_f32 v[40:41], v[108:109], v[12:13]
	v_pk_mul_f32 v[38:39], v[106:107], v[10:11]
	v_pk_mul_f32 v[36:37], v[112:113], v[16:17]
	v_pk_mul_f32 v[34:35], v[110:111], v[14:15]

; #define GAS __attribute__((address_space(1)))
; __device__ __forceinline__ unsigned pk2(float lo, float hi) { unsigned r; asm("v_cvt_pk_bf16_f32 %0, %1, %2" : "=v"(r) : "v"(lo), "v"(hi)); return r; }
; __device__ __forceinline__ bf16_t* x_row_ptr(Frame& F, int row) { return (bf16_t*)(F.ws + WS_X) + (size_t)row * D; }
; #define N1_STEP0(XC, XI, kk) do { const int k_ = (kk), row_ = rbeg + k_; N1_MOD(row_); N1_XLD(XI, rbeg + (k_ + 2 < RPW ? k_ + 2 : RPW - 1)); n1_finish(F, L, row_, XC, gs, sh); } while (0)
; __device__ __forceinline__ void n1_finish(Frame& F, int L, int row, const f32x4 (&v)[4], const f32x4 (&gs)[4], const f32x4 (&sh)[4]) {
;     bf16_t* H = (bf16_t*)(F.ws + WS_H);
;     x_store_row(x_row_ptr(F, row), F.lane, v);
;     float ss = 0.f;
; #pragma unroll
;     for (int j = 0; j < 4; ++j) ss += (v[j][0] * v[j][0] + v[j][1] * v[j][1]) + (v[j][2] * v[j][2] + v[j][3] * v[j][3]);
;     const float rinv = __builtin_amdgcn_rsqf(wave_sum(ss) * (1.0f / D) + EPS);
;     if ((L & 1) == 0) {
;         GAS unsigned* o4 = (GAS unsigned*)((unsigned char*)H + (size_t)row * D) + F.lane;
; #pragma unroll
;         for (int j = 0; j < 4; ++j) { const f32x4 h = ((v[j] * rinv) * gs[j] + sh[j]) * pg8::SC_H2; o4[64 * j] = pg8::pack4_fp8(h[0], h[1], h[2], h[3]); }
;     } else {
;         GAS u32x2* o8 = (GAS u32x2*)(H + (size_t)row * D) + F.lane;
; #pragma unroll
;         for (int j = 0; j < 4; ++j) { const f32x4 h = (v[j] * rinv) * gs[j] + sh[j]; u32x2 w; w.x = pk2(h[0], h[1]); w.y = pk2(h[2], h[3]); o8[64 * j] = w; }
;     }
; }
; __device__ __forceinline__ void n1_phase(const Frame& F0, int L, int nrows) {
;     ...
;         for (; k + 2 < RPW; k += 3) { N1_STEP0(X0, X2, k); N1_STEP0(X1, X0, k + 1); N1_STEP0(X2, X1, k + 2); }
.LBB0_393:
	s_waitcnt vmcnt(23)
	v_pk_mul_f32 v[2:3], v[80:81], v[80:81]
	v_pk_mul_f32 v[4:5], v[78:79], v[78:79]
	s_waitcnt vmcnt(20)
	v_mul_f32_e32 v1, v66, v66
	v_pk_mov_b32 v[6:7], v[4:5], v[2:3] op_sel:[1,0]
	v_mov_b32_e32 v5, v3
	v_pk_add_f32 v[2:3], v[6:7], v[4:5]
	v_pk_mul_f32 v[4:5], v[76:77], v[76:77]
	v_pk_mul_f32 v[6:7], v[74:75], v[74:75]
	v_pk_add_f32 v[2:3], v[2:3], v[2:3] op_sel:[0,1] op_sel_hi:[1,0]
	v_pk_mov_b32 v[8:9], v[6:7], v[4:5] op_sel:[1,0]
	v_mov_b32_e32 v7, v5
	v_pk_add_f32 v[4:5], v[8:9], v[6:7]
	v_mul_f32_e32 v6, v67, v67
	v_pk_add_f32 v[4:5], v[4:5], v[4:5] op_sel:[0,1] op_sel_hi:[1,0]
	v_mov_b32_e32 v3, v1
	v_mov_b32_e32 v5, v6
	v_pk_add_f32 v[2:3], v[2:3], v[4:5]
	v_mul_f32_e32 v4, v71, v71
	v_mul_f32_e32 v7, v68, v68
	v_pk_fma_f32 v[4:5], v[70:71], v[70:71], v[4:5] op_sel_hi:[1,1,0]
	v_mul_f32_e32 v6, v73, v73
	v_mul_f32_e32 v8, v69, v69
	v_mov_b32_e32 v5, v7
	v_pk_fma_f32 v[6:7], v[72:73], v[72:73], v[6:7] op_sel_hi:[1,1,0]
	s_lshl_b64 s[4:5], s[4:5], 12
	v_mov_b32_e32 v7, v8
	v_pk_add_f32 v[4:5], v[4:5], v[6:7]
	s_add_u32 s2, s2, s4
	v_pk_add_f32 v[2:3], v[2:3], v[4:5]
	s_addc_u32 s3, s3, s5
	v_add_f32_e32 v1, v2, v3
	global_load_dwordx4 v[14:17], v84, s[2:3] nt
	global_load_dwordx4 v[10:13], v84, s[2:3] offset:1024 nt
	s_ashr_i32 s1, s0, 31
	v_readlane_b32 s4, v255, 22
	s_waitcnt lgkmcnt(0)
	s_nop 1
	v_mov_b32_dpp v2, v1 quad_perm:[1,0,3,2] row_mask:0xf bank_mask:0xf
	v_add_f32_e32 v1, v1, v2
	s_waitcnt lgkmcnt(0)
	s_nop 1
	v_mov_b32_dpp v2, v1 quad_perm:[2,3,0,1] row_mask:0xf bank_mask:0xf
	v_add_f32_e32 v1, v1, v2
	global_load_dwordx4 v[6:9], v84, s[2:3] offset:2048 nt
	global_load_dwordx4 v[2:5], v84, s[2:3] offset:3072 nt
	v_cvt_pk_bf16_f32 v102, v78, v79
	s_lshl_b64 s[2:3], s[0:1], 11
	v_lshl_add_u64 v[106:107], v[94:95], 0, s[2:3]
	s_lshl_b64 s[0:1], s[0:1], 10
	s_waitcnt lgkmcnt(0)
	s_nop 1
	v_mov_b32_dpp v83, v1 row_half_mirror row_mask:0xf bank_mask:0xf
	v_add_f32_e32 v1, v1, v83
	v_cvt_pk_bf16_f32 v103, v80, v81
	global_store_dwordx2 v[106:107], v[102:103], off
	v_cvt_pk_bf16_f32 v102, v74, v75
	v_cvt_pk_bf16_f32 v103, v76, v77
	s_waitcnt lgkmcnt(0)
	s_nop 1
	v_mov_b32_dpp v83, v1 row_mirror row_mask:0xf bank_mask:0xf
	v_add_f32_e32 v1, v1, v83
	global_store_dwordx2 v[106:107], v[102:103], off offset:512
	v_cvt_pk_bf16_f32 v102, v70, v71
	v_cvt_pk_bf16_f32 v103, v72, v73
	global_store_dwordx2 v[106:107], v[102:103], off offset:1024
	s_waitcnt lgkmcnt(0)
	v_mov_b32_e32 v83, v1
	s_nop 1
	v_permlane16_swap_b32_e32 v83, v1
	v_add_f32_e32 v1, v1, v83
	v_cvt_pk_bf16_f32 v102, v66, v67
	v_cvt_pk_bf16_f32 v103, v68, v69
	s_mov_b64 s[2:3], 0xc00
	global_store_dwordx2 v[106:107], v[102:103], off offset:1536
	s_waitcnt lgkmcnt(0)
	v_mov_b32_e32 v83, v1
	s_nop 1
	v_permlane32_swap_b32_e32 v83, v1
	v_add_f32_e32 v1, v1, v83
	v_fmamk_f32 v1, v1, 0x3a800000, v250
	v_rsq_f32_e32 v104, v1
	v_mov_b32_e32 v83, v191
	v_lshl_add_u64 v[102:103], v[96:97], 0, s[0:1]
	s_add_i32 s0, s19, 3
	v_pk_mul_f32 v[78:79], v[78:79], v[104:105] op_sel_hi:[1,0]
	v_pk_mul_f32 v[80:81], v[80:81], v[104:105] op_sel_hi:[1,0]
	v_pk_fma_f32 v[78:79], v[50:51], v[78:79], v[26:27]
	v_pk_fma_f32 v[80:81], v[52:53], v[80:81], v[28:29]
	v_pk_mul_f32 v[78:79], v[78:79], s[16:17] op_sel_hi:[1,0]
	v_pk_mul_f32 v[74:75], v[74:75], v[104:105] op_sel_hi:[1,0]
	v_med3_f32 v1, v78, s15, v212
	v_med3_f32 v78, v79, s15, v212
	v_cvt_pk_fp8_f32 v83, v1, v78
	v_pk_mul_f32 v[78:79], v[80:81], s[16:17] op_sel_hi:[1,0]
	v_pk_fma_f32 v[74:75], v[42:43], v[74:75], v[22:23]
	v_med3_f32 v1, v78, s15, v212
	v_med3_f32 v78, v79, s15, v212
	v_pk_mul_f32 v[74:75], v[74:75], s[16:17] op_sel_hi:[1,0]
	v_cvt_pk_fp8_f32 v83, v1, v78 op_sel:[0,0,1]
	v_med3_f32 v1, v74, s15, v212
	v_med3_f32 v74, v75, s15, v212
	v_mov_b32_e32 v78, v191
	v_pk_mul_f32 v[76:77], v[76:77], v[104:105] op_sel_hi:[1,0]
	v_cvt_pk_fp8_f32 v78, v1, v74
	v_pk_fma_f32 v[76:77], v[44:45], v[76:77], v[24:25]
	v_pk_mul_f32 v[70:71], v[70:71], v[104:105] op_sel_hi:[1,0]
	v_pk_mul_f32 v[74:75], v[76:77], s[16:17] op_sel_hi:[1,0]
	v_pk_fma_f32 v[70:71], v[38:39], v[70:71], v[18:19]
	v_med3_f32 v1, v74, s15, v212
	v_med3_f32 v74, v75, s15, v212
	v_pk_mul_f32 v[70:71], v[70:71], s[16:17] op_sel_hi:[1,0]
	v_cvt_pk_fp8_f32 v78, v1, v74 op_sel:[0,0,1]
	v_med3_f32 v1, v70, s15, v212
	v_med3_f32 v70, v71, s15, v212
	v_mov_b32_e32 v74, v191
	v_pk_mul_f32 v[72:73], v[72:73], v[104:105] op_sel_hi:[1,0]
	v_cvt_pk_fp8_f32 v74, v1, v70
	v_pk_fma_f32 v[72:73], v[40:41], v[72:73], v[20:21]
	v_pk_mul_f32 v[66:67], v[66:67], v[104:105] op_sel_hi:[1,0]
	v_pk_mul_f32 v[70:71], v[72:73], s[16:17] op_sel_hi:[1,0]
	v_pk_fma_f32 v[66:67], v[34:35], v[66:67], v[30:31]
	v_med3_f32 v1, v70, s15, v212
	v_med3_f32 v70, v71, s15, v212
	v_pk_mul_f32 v[66:67], v[66:67], s[16:17] op_sel_hi:[1,0]
	v_cvt_pk_fp8_f32 v74, v1, v70 op_sel:[0,0,1]
	v_med3_f32 v1, v66, s15, v212
	v_med3_f32 v66, v67, s15, v212
	v_mov_b32_e32 v70, v191
	v_pk_mul_f32 v[68:69], v[68:69], v[104:105] op_sel_hi:[1,0]
	v_cvt_pk_fp8_f32 v70, v1, v66
	v_pk_fma_f32 v[68:69], v[36:37], v[68:69], v[32:33]
	s_add_i32 s1, s19, 1
	v_pk_mul_f32 v[66:67], v[68:69], s[16:17] op_sel_hi:[1,0]
	v_lshl_add_u64 v[98:99], v[98:99], 0, s[2:3]
	v_med3_f32 v1, v66, s15, v212
	v_med3_f32 v66, v67, s15, v212
	s_mov_b64 s[2:3], 0x1800
	v_cvt_pk_fp8_f32 v70, v1, v66 op_sel:[0,0,1]
	s_cmp_lt_i32 s1, s4
	v_lshl_add_u64 v[100:101], v[100:101], 0, s[2:3]
	global_store_dword v[102:103], v83, off
	global_store_dword v[102:103], v78, off offset:256
	global_store_dword v[102:103], v74, off offset:512
	global_store_dword v[102:103], v70, off offset:768
	s_cbranch_scc0 .LBB0_396
	s_mov_b32 s19, s0
	s_branch .LBB0_375

; #define GAS __attribute__((address_space(1)))
; __device__ __forceinline__ unsigned pk2(float lo, float hi) { unsigned r; asm("v_cvt_pk_bf16_f32 %0, %1, %2" : "=v"(r) : "v"(lo), "v"(hi)); return r; }
; __device__ __forceinline__ bf16_t* x_row_ptr(Frame& F, int row) { return (bf16_t*)(F.ws + WS_X) + (size_t)row * D; }
; #define N1_STEP0(XC, XI, kk) do { const int k_ = (kk), row_ = rbeg + k_; N1_MOD(row_); N1_XLD(XI, rbeg + (k_ + 2 < RPW ? k_ + 2 : RPW - 1)); n1_finish(F, L, row_, XC, gs, sh); } while (0)
; __device__ __forceinline__ void n1_finish(Frame& F, int L, int row, const f32x4 (&v)[4], const f32x4 (&gs)[4], const f32x4 (&sh)[4]) {
;     bf16_t* H = (bf16_t*)(F.ws + WS_H);
;     x_store_row(x_row_ptr(F, row), F.lane, v);
;     float ss = 0.f;
; #pragma unroll
;     for (int j = 0; j < 4; ++j) ss += (v[j][0] * v[j][0] + v[j][1] * v[j][1]) + (v[j][2] * v[j][2] + v[j][3] * v[j][3]);
;     const float rinv = __builtin_amdgcn_rsqf(wave_sum(ss) * (1.0f / D) + EPS);
;     if ((L & 1) == 0) {
;         GAS unsigned* o4 = (GAS unsigned*)((unsigned char*)H + (size_t)row * D) + F.lane;
; #pragma unroll
;         for (int j = 0; j < 4; ++j) { const f32x4 h = ((v[j] * rinv) * gs[j] + sh[j]) * pg8::SC_H2; o4[64 * j] = pg8::pack4_fp8(h[0], h[1], h[2], h[3]); }
;     } else {
;         GAS u32x2* o8 = (GAS u32x2*)(H + (size_t)row * D) + F.lane;
; #pragma unroll
;         for (int j = 0; j < 4; ++j) { const f32x4 h = (v[j] * rinv) * gs[j] + sh[j]; u32x2 w; w.x = pk2(h[0], h[1]); w.y = pk2(h[2], h[3]); o8[64 * j] = w; }
;     }
; }
; __device__ __forceinline__ void n1_phase(const Frame& F0, int L, int nrows) {
;     ...
;         if (k < RPW) { N1_STEP0(X0, X2, k); if (k + 1 < RPW) N1_STEP0(X1, X0, k + 1); }
.LBB0_399:
	s_waitcnt vmcnt(7)
	v_pk_mul_f32 v[66:67], v[64:65], v[64:65]
	v_pk_mul_f32 v[68:69], v[62:63], v[62:63]
	v_and_b32_e32 v1, 64, v211
	v_pk_mov_b32 v[70:71], v[68:69], v[66:67] op_sel:[1,0]
	v_mov_b32_e32 v69, v67
	v_pk_add_f32 v[66:67], v[70:71], v[68:69]
	s_waitcnt vmcnt(6)
	v_pk_mul_f32 v[68:69], v[60:61], v[60:61]
	v_pk_add_f32 v[66:67], v[66:67], v[66:67] op_sel_hi:[0,1]
	v_pk_mul_f32 v[70:71], v[58:59], v[58:59]
	s_waitcnt vmcnt(5)
	v_mul_f32_e32 v66, v54, v54
	v_pk_mov_b32 v[72:73], v[70:71], v[68:69] op_sel:[1,0]
	v_mov_b32_e32 v71, v69
	v_pk_add_f32 v[68:69], v[72:73], v[70:71]
	v_pk_fma_f32 v[70:71], v[54:55], v[54:55], v[66:67] op_sel_hi:[1,1,0]
	v_mul_f32_e32 v66, v56, v56
	v_pk_fma_f32 v[72:73], v[56:57], v[56:57], v[66:67] op_sel_hi:[1,1,0]
	v_pk_add_f32 v[68:69], v[68:69], v[68:69] op_sel_hi:[0,1]
	s_waitcnt vmcnt(4)
	v_mul_f32_e32 v70, v46, v46
	v_mul_f32_e32 v72, v47, v47
	v_mul_f32_e32 v68, v48, v48
	v_mul_f32_e32 v66, v49, v49
	v_pk_add_f32 v[70:71], v[70:71], v[72:73]
	v_add_u32_e32 v72, 64, v1
	v_xor_b32_e32 v1, 1, v211
	v_pk_add_f32 v[66:67], v[68:69], v[66:67]
	v_cmp_lt_i32_e32 vcc, v1, v72
	v_pk_add_f32 v[66:67], v[70:71], v[66:67]
	s_ashr_i32 s1, s0, 31
	v_cndmask_b32_e32 v1, v211, v1, vcc
	v_add_f32_e32 v66, v66, v67
	v_lshlrev_b32_e32 v1, 2, v1
	s_lshl_b64 s[2:3], s[0:1], 11
	v_readlane_b32 s4, v252, 20
	v_readlane_b32 s5, v252, 21
	s_add_u32 s2, s4, s2
	s_waitcnt lgkmcnt(0)
	s_nop 1
	v_mov_b32_dpp v67, v66 quad_perm:[1,0,3,2] row_mask:0xf bank_mask:0xf
	v_add_f32_e32 v67, v66, v67
	v_xor_b32_e32 v66, 2, v211
	v_cmp_lt_i32_e32 vcc, v66, v72
	s_addc_u32 s3, s5, s3
	v_cvt_pk_bf16_f32 v70, v62, v63
	v_cvt_pk_bf16_f32 v71, v64, v65
	global_store_dwordx2 v82, v[70:71], s[2:3]
	v_cndmask_b32_e32 v66, v211, v66, vcc
	v_lshlrev_b32_e32 v66, 2, v66
	v_cvt_pk_bf16_f32 v70, v58, v59
	v_cvt_pk_bf16_f32 v71, v60, v61
	global_store_dwordx2 v82, v[70:71], s[2:3] offset:512
	v_xor_b32_e32 v70, 32, v211
	s_waitcnt lgkmcnt(0)
	s_nop 1
	v_mov_b32_dpp v68, v67 quad_perm:[2,3,0,1] row_mask:0xf bank_mask:0xf
	v_add_f32_e32 v67, v67, v68
	v_xor_b32_e32 v68, 4, v211
	v_cmp_lt_i32_e32 vcc, v68, v72
	s_lshl_b64 s[0:1], s[0:1], 10
	s_nop 0
	v_cndmask_b32_e32 v68, v211, v68, vcc
	v_lshlrev_b32_e32 v68, 2, v68
	s_waitcnt lgkmcnt(0)
	s_nop 1
	v_mov_b32_dpp v69, v67 row_half_mirror row_mask:0xf bank_mask:0xf
	v_add_f32_e32 v69, v67, v69
	v_xor_b32_e32 v67, 8, v211
	v_cmp_lt_i32_e32 vcc, v67, v72
	s_nop 1
	v_cndmask_b32_e32 v67, v211, v67, vcc
	v_lshlrev_b32_e32 v67, 2, v67
	s_waitcnt lgkmcnt(0)
	s_nop 1
	v_mov_b32_dpp v73, v69 row_mirror row_mask:0xf bank_mask:0xf
	v_add_f32_e32 v73, v69, v73
	v_xor_b32_e32 v69, 16, v211
	v_cmp_lt_i32_e32 vcc, v69, v72
	s_nop 1
	v_cndmask_b32_e32 v69, v211, v69, vcc
	v_lshlrev_b32_e32 v69, 2, v69
	v_cmp_lt_i32_e32 vcc, v70, v72
	v_cvt_pk_bf16_f32 v72, v54, v55
	s_waitcnt lgkmcnt(0)
	v_mov_b32_e32 v74, v73
	v_mov_b32_e32 v71, v73
	s_nop 1
	v_permlane16_swap_b32_e32 v74, v71
	v_add_f32_e32 v71, v71, v74
	v_cndmask_b32_e32 v70, v211, v70, vcc
	v_lshlrev_b32_e32 v70, 2, v70
	v_cvt_pk_bf16_f32 v73, v56, v57
	global_store_dwordx2 v82, v[72:73], s[2:3] offset:1024
	v_cvt_pk_bf16_f32 v72, v46, v47
	v_cvt_pk_bf16_f32 v73, v48, v49
	s_waitcnt lgkmcnt(0)
	v_mov_b32_e32 v74, v71
	s_nop 1
	v_permlane32_swap_b32_e32 v74, v71
	v_add_f32_e32 v71, v71, v74
	v_fmamk_f32 v71, v71, 0x3a800000, v250
	v_rsq_f32_e32 v74, v71
	v_mov_b32_e32 v71, v191
	global_store_dwordx2 v82, v[72:73], s[2:3] offset:1536
	s_add_u32 s2, s96, s0
	v_pk_mul_f32 v[62:63], v[62:63], v[74:75] op_sel_hi:[1,0]
	v_pk_mul_f32 v[64:65], v[64:65], v[74:75] op_sel_hi:[1,0]
	v_pk_fma_f32 v[62:63], v[50:51], v[62:63], v[26:27]
	v_pk_fma_f32 v[64:65], v[52:53], v[64:65], v[28:29]
	v_pk_mul_f32 v[62:63], v[62:63], s[16:17] op_sel_hi:[1,0]
	v_pk_mul_f32 v[58:59], v[58:59], v[74:75] op_sel_hi:[1,0]
	v_med3_f32 v62, v62, s15, v212
	v_med3_f32 v63, v63, s15, v212
	v_cvt_pk_fp8_f32 v71, v62, v63
	v_pk_mul_f32 v[62:63], v[64:65], s[16:17] op_sel_hi:[1,0]
	v_pk_fma_f32 v[58:59], v[42:43], v[58:59], v[22:23]
	v_med3_f32 v62, v62, s15, v212
	v_med3_f32 v63, v63, s15, v212
	v_pk_mul_f32 v[58:59], v[58:59], s[16:17] op_sel_hi:[1,0]
	v_cvt_pk_fp8_f32 v71, v62, v63 op_sel:[0,0,1]
	v_med3_f32 v58, v58, s15, v212
	v_med3_f32 v59, v59, s15, v212
	v_mov_b32_e32 v62, v191
	v_pk_mul_f32 v[60:61], v[60:61], v[74:75] op_sel_hi:[1,0]
	v_cvt_pk_fp8_f32 v62, v58, v59
	v_pk_fma_f32 v[60:61], v[44:45], v[60:61], v[24:25]
	v_pk_mul_f32 v[54:55], v[54:55], v[74:75] op_sel_hi:[1,0]
	v_pk_mul_f32 v[58:59], v[60:61], s[16:17] op_sel_hi:[1,0]
	v_pk_fma_f32 v[54:55], v[38:39], v[54:55], v[18:19]
	v_med3_f32 v58, v58, s15, v212
	v_med3_f32 v59, v59, s15, v212
	v_pk_mul_f32 v[54:55], v[54:55], s[16:17] op_sel_hi:[1,0]
	v_cvt_pk_fp8_f32 v62, v58, v59 op_sel:[0,0,1]
	v_med3_f32 v54, v54, s15, v212
	v_med3_f32 v55, v55, s15, v212
	v_mov_b32_e32 v58, v191
	v_pk_mul_f32 v[56:57], v[56:57], v[74:75] op_sel_hi:[1,0]
	v_cvt_pk_fp8_f32 v58, v54, v55
	v_pk_fma_f32 v[56:57], v[40:41], v[56:57], v[20:21]
	v_pk_mul_f32 v[46:47], v[46:47], v[74:75] op_sel_hi:[1,0]
	v_pk_mul_f32 v[54:55], v[56:57], s[16:17] op_sel_hi:[1,0]
	v_pk_fma_f32 v[46:47], v[34:35], v[46:47], v[30:31]
	v_med3_f32 v54, v54, s15, v212
	v_med3_f32 v55, v55, s15, v212
	v_pk_mul_f32 v[46:47], v[46:47], s[16:17] op_sel_hi:[1,0]
	v_cvt_pk_fp8_f32 v58, v54, v55 op_sel:[0,0,1]
	v_med3_f32 v46, v46, s15, v212
	v_med3_f32 v47, v47, s15, v212
	v_mov_b32_e32 v54, v191
	v_pk_mul_f32 v[48:49], v[48:49], v[74:75] op_sel_hi:[1,0]
	v_cvt_pk_fp8_f32 v54, v46, v47
	v_pk_fma_f32 v[48:49], v[36:37], v[48:49], v[32:33]
	s_addc_u32 s3, s97, s1
	v_pk_mul_f32 v[46:47], v[48:49], s[16:17] op_sel_hi:[1,0]
	s_add_i32 s0, s22, 1
	v_med3_f32 v46, v46, s15, v212
	v_med3_f32 v47, v47, s15, v212
	v_cvt_pk_fp8_f32 v54, v46, v47 op_sel:[0,0,1]
	v_readlane_b32 s1, v255, 22
	s_cmp_ge_i32 s0, s1
	global_store_dword v190, v71, s[2:3]
	global_store_dword v190, v62, s[2:3] offset:256
	global_store_dword v190, v58, s[2:3] offset:512
	global_store_dword v190, v54, s[2:3] offset:768
	s_cbranch_scc1 .LBB0_403
; #define GAS __attribute__((address_space(1)))
; __device__ __forceinline__ unsigned pk2(float lo, float hi) { unsigned r; asm("v_cvt_pk_bf16_f32 %0, %1, %2" : "=v"(r) : "v"(lo), "v"(hi)); return r; }
; __device__ __forceinline__ bf16_t* x_row_ptr(Frame& F, int row) { return (bf16_t*)(F.ws + WS_X) + (size_t)row * D; }
; __device__ __forceinline__ void n1_finish(Frame& F, int L, int row, const f32x4 (&v)[4], const f32x4 (&gs)[4], const f32x4 (&sh)[4]) {
;     bf16_t* H = (bf16_t*)(F.ws + WS_H);
;     x_store_row(x_row_ptr(F, row), F.lane, v);
;     float ss = 0.f;
; #pragma unroll
;     for (int j = 0; j < 4; ++j) ss += (v[j][0] * v[j][0] + v[j][1] * v[j][1]) + (v[j][2] * v[j][2] + v[j][3] * v[j][3]);
;     const float rinv = __builtin_amdgcn_rsqf(wave_sum(ss) * (1.0f / D) + EPS);
;     if ((L & 1) == 0) {
;         GAS unsigned* o4 = (GAS unsigned*)((unsigned char*)H + (size_t)row * D) + F.lane;
; #pragma unroll
;         for (int j = 0; j < 4; ++j) { const f32x4 h = ((v[j] * rinv) * gs[j] + sh[j]) * pg8::SC_H2; o4[64 * j] = pg8::pack4_fp8(h[0], h[1], h[2], h[3]); }
;     } else {
;         GAS u32x2* o8 = (GAS u32x2*)(H + (size_t)row * D) + F.lane;
; #pragma unroll
;         for (int j = 0; j < 4; ++j) { const f32x4 h = (v[j] * rinv) * gs[j] + sh[j]; u32x2 w; w.x = pk2(h[0], h[1]); w.y = pk2(h[2], h[3]); o8[64 * j] = w; }
;     }
; }
	s_add_i32 s0, s0, s38
	s_min_i32 s1, s0, 0x8000
	s_ashr_i32 s1, s1, 11
	s_cmp_eq_u32 s1, s17
	s_cbranch_scc1 .LBB0_402
	s_mul_i32 s2, s1, 0x1800
	s_ashr_i32 s3, s2, 31
	s_lshl_b64 s[2:3], s[2:3], 2
	v_readlane_b32 s1, v255, 20
	s_add_u32 s2, s1, s2
	v_readlane_b32 s1, v255, 21
	s_addc_u32 s3, s1, s3
	s_add_u32 s4, s2, 0x1000
	s_addc_u32 s5, s3, 0
	v_or_b32_e32 v18, 0x400, v84
	global_load_dwordx4 v[34:37], v84, s[4:5]
	global_load_dwordx4 v[38:41], v18, s[4:5]
	v_or_b32_e32 v18, 0x800, v84
	global_load_dwordx4 v[42:45], v18, s[4:5]
	v_or_b32_e32 v18, 0xc00, v84
	global_load_dwordx4 v[46:49], v18, s[4:5]
	v_mov_b32_e32 v85, v191
	v_lshl_add_u64 v[18:19], s[28:29], 0, v[84:85]
	flat_load_dwordx4 v[50:53], v[18:19]
	flat_load_dwordx4 v[54:57], v[18:19] offset:1024
	flat_load_dwordx4 v[58:61], v[18:19] offset:2048
	flat_load_dwordx4 v[62:65], v[18:19] offset:3072
	global_load_dwordx4 v[22:25], v84, s[2:3] offset:1024 nt
	s_nop 0
	global_load_dwordx4 v[18:21], v84, s[2:3] offset:2048 nt
	global_load_dwordx4 v[26:29], v84, s[2:3] nt
	global_load_dwordx4 v[30:33], v84, s[2:3] offset:3072 nt
	s_waitcnt vmcnt(0)
	v_pk_add_f32 v[36:37], v[36:37], 1.0 op_sel_hi:[1,0]
	v_pk_add_f32 v[34:35], v[34:35], 1.0 op_sel_hi:[1,0]
	v_pk_add_f32 v[40:41], v[40:41], 1.0 op_sel_hi:[1,0]
	v_pk_add_f32 v[38:39], v[38:39], 1.0 op_sel_hi:[1,0]
	v_pk_add_f32 v[72:73], v[44:45], 1.0 op_sel_hi:[1,0]
	v_pk_add_f32 v[74:75], v[42:43], 1.0 op_sel_hi:[1,0]
	v_pk_add_f32 v[48:49], v[48:49], 1.0 op_sel_hi:[1,0]
	v_pk_add_f32 v[46:47], v[46:47], 1.0 op_sel_hi:[1,0]
	s_waitcnt lgkmcnt(0)
	v_pk_mul_f32 v[52:53], v[52:53], v[36:37]
	v_pk_mul_f32 v[50:51], v[50:51], v[34:35]
	v_pk_mul_f32 v[44:45], v[56:57], v[40:41]
	v_pk_mul_f32 v[42:43], v[54:55], v[38:39]
	v_pk_mul_f32 v[40:41], v[60:61], v[72:73]
	v_pk_mul_f32 v[38:39], v[58:59], v[74:75]
	v_pk_mul_f32 v[36:37], v[64:65], v[48:49]
	v_pk_mul_f32 v[34:35], v[62:63], v[46:47]
.LBB0_402:
	s_waitcnt vmcnt(11)
	v_pk_mul_f32 v[46:47], v[16:17], v[16:17]
	v_pk_mul_f32 v[48:49], v[14:15], v[14:15]
	s_ashr_i32 s1, s0, 31
	v_pk_mov_b32 v[54:55], v[48:49], v[46:47] op_sel:[1,0]
	v_mov_b32_e32 v49, v47
	v_pk_add_f32 v[46:47], v[54:55], v[48:49]
	s_waitcnt vmcnt(10)
	v_pk_mul_f32 v[48:49], v[12:13], v[12:13]
	v_pk_add_f32 v[46:47], v[46:47], v[46:47] op_sel_hi:[0,1]
	v_pk_mul_f32 v[54:55], v[10:11], v[10:11]
	s_waitcnt vmcnt(9)
	v_mul_f32_e32 v46, v6, v6
	v_pk_mov_b32 v[56:57], v[54:55], v[48:49] op_sel:[1,0]
	v_mov_b32_e32 v55, v49
	v_pk_add_f32 v[48:49], v[56:57], v[54:55]
	v_pk_fma_f32 v[54:55], v[6:7], v[6:7], v[46:47] op_sel_hi:[1,1,0]
	v_mul_f32_e32 v46, v8, v8
	v_pk_add_f32 v[48:49], v[48:49], v[48:49] op_sel_hi:[0,1]
	v_pk_fma_f32 v[56:57], v[8:9], v[8:9], v[46:47] op_sel_hi:[1,1,0]
	s_waitcnt vmcnt(8)
	v_mul_f32_e32 v54, v2, v2
	v_mul_f32_e32 v56, v3, v3
	v_mul_f32_e32 v48, v4, v4
	v_mul_f32_e32 v46, v5, v5
	v_pk_add_f32 v[54:55], v[54:55], v[56:57]
	v_pk_add_f32 v[46:47], v[48:49], v[46:47]
	s_lshl_b64 s[2:3], s[0:1], 11
	v_pk_add_f32 v[46:47], v[54:55], v[46:47]
	v_readlane_b32 s4, v252, 20
	v_add_f32_e32 v46, v46, v47
	v_readlane_b32 s5, v252, 21
	s_add_u32 s2, s4, s2
	s_addc_u32 s3, s5, s3
	v_cvt_pk_bf16_f32 v47, v16, v17
	s_waitcnt lgkmcnt(0)
	s_nop 1
	v_mov_b32_dpp v1, v46 quad_perm:[1,0,3,2] row_mask:0xf bank_mask:0xf
	v_add_f32_e32 v1, v46, v1
	s_lshl_b64 s[0:1], s[0:1], 10
	s_add_u32 s0, s96, s0
	s_addc_u32 s1, s97, s1
	s_waitcnt lgkmcnt(0)
	s_nop 1
	v_mov_b32_dpp v46, v1 quad_perm:[2,3,0,1] row_mask:0xf bank_mask:0xf
	v_add_f32_e32 v1, v1, v46
	s_waitcnt lgkmcnt(0)
	s_nop 1
	v_mov_b32_dpp v46, v1 row_half_mirror row_mask:0xf bank_mask:0xf
	v_add_f32_e32 v1, v1, v46
	v_cvt_pk_bf16_f32 v46, v14, v15
	global_store_dwordx2 v82, v[46:47], s[2:3]
	v_cvt_pk_bf16_f32 v46, v10, v11
	v_cvt_pk_bf16_f32 v47, v12, v13
	s_waitcnt lgkmcnt(0)
	s_nop 1
	v_mov_b32_dpp v48, v1 row_mirror row_mask:0xf bank_mask:0xf
	v_add_f32_e32 v1, v1, v48
	global_store_dwordx2 v82, v[46:47], s[2:3] offset:512
	v_cvt_pk_bf16_f32 v46, v6, v7
	v_cvt_pk_bf16_f32 v47, v8, v9
	global_store_dwordx2 v82, v[46:47], s[2:3] offset:1024
	s_waitcnt lgkmcnt(0)
	v_mov_b32_e32 v48, v1
	s_nop 1
	v_permlane16_swap_b32_e32 v48, v1
	v_add_f32_e32 v1, v1, v48
	v_cvt_pk_bf16_f32 v46, v2, v3
	v_cvt_pk_bf16_f32 v47, v4, v5
	global_store_dwordx2 v82, v[46:47], s[2:3] offset:1536
	s_waitcnt lgkmcnt(0)
	v_mov_b32_e32 v48, v1
	s_nop 1
	v_permlane32_swap_b32_e32 v48, v1
	v_add_f32_e32 v1, v1, v48
	v_fmamk_f32 v1, v1, 0x3a800000, v250
	v_rsq_f32_e32 v46, v1
	s_nop 0
	v_pk_mul_f32 v[14:15], v[14:15], v[46:47] op_sel_hi:[1,0]
	s_nop 0
	v_pk_fma_f32 v[14:15], v[50:51], v[14:15], v[26:27]
	v_mov_b32_e32 v26, v191
	v_pk_mul_f32 v[14:15], v[14:15], s[16:17] op_sel_hi:[1,0]
	v_pk_mul_f32 v[16:17], v[16:17], v[46:47] op_sel_hi:[1,0]
	v_med3_f32 v1, v14, s15, v212
	v_med3_f32 v14, v15, s15, v212
	v_cvt_pk_fp8_f32 v26, v1, v14
	v_pk_fma_f32 v[16:17], v[52:53], v[16:17], v[28:29]
	v_pk_mul_f32 v[10:11], v[10:11], v[46:47] op_sel_hi:[1,0]
	v_pk_mul_f32 v[14:15], v[16:17], s[16:17] op_sel_hi:[1,0]
	v_pk_fma_f32 v[10:11], v[42:43], v[10:11], v[22:23]
	v_med3_f32 v1, v14, s15, v212
	v_med3_f32 v14, v15, s15, v212
	v_pk_mul_f32 v[10:11], v[10:11], s[16:17] op_sel_hi:[1,0]
	v_cvt_pk_fp8_f32 v26, v1, v14 op_sel:[0,0,1]
	v_med3_f32 v1, v10, s15, v212
	v_med3_f32 v10, v11, s15, v212
	v_mov_b32_e32 v14, v191
	v_pk_mul_f32 v[12:13], v[12:13], v[46:47] op_sel_hi:[1,0]
	v_cvt_pk_fp8_f32 v14, v1, v10
	v_pk_fma_f32 v[12:13], v[44:45], v[12:13], v[24:25]
	v_pk_mul_f32 v[6:7], v[6:7], v[46:47] op_sel_hi:[1,0]
	v_pk_mul_f32 v[10:11], v[12:13], s[16:17] op_sel_hi:[1,0]
	v_pk_fma_f32 v[6:7], v[38:39], v[6:7], v[18:19]
	v_med3_f32 v1, v10, s15, v212
	v_med3_f32 v10, v11, s15, v212
	v_pk_mul_f32 v[6:7], v[6:7], s[16:17] op_sel_hi:[1,0]
	v_cvt_pk_fp8_f32 v14, v1, v10 op_sel:[0,0,1]
	v_med3_f32 v1, v6, s15, v212
	v_med3_f32 v6, v7, s15, v212
	v_mov_b32_e32 v10, v191
	v_pk_mul_f32 v[8:9], v[8:9], v[46:47] op_sel_hi:[1,0]
	v_cvt_pk_fp8_f32 v10, v1, v6
	v_pk_fma_f32 v[8:9], v[40:41], v[8:9], v[20:21]
	v_pk_mul_f32 v[2:3], v[2:3], v[46:47] op_sel_hi:[1,0]
	v_pk_mul_f32 v[6:7], v[8:9], s[16:17] op_sel_hi:[1,0]
	v_pk_fma_f32 v[2:3], v[34:35], v[2:3], v[30:31]
	v_med3_f32 v1, v6, s15, v212
	v_med3_f32 v6, v7, s15, v212
	v_pk_mul_f32 v[2:3], v[2:3], s[16:17] op_sel_hi:[1,0]
	v_cvt_pk_fp8_f32 v10, v1, v6 op_sel:[0,0,1]
	v_med3_f32 v1, v2, s15, v212
	v_med3_f32 v2, v3, s15, v212
	v_mov_b32_e32 v6, v191
	v_pk_mul_f32 v[4:5], v[4:5], v[46:47] op_sel_hi:[1,0]
	v_cvt_pk_fp8_f32 v6, v1, v2
	v_pk_fma_f32 v[4:5], v[36:37], v[4:5], v[32:33]
	s_nop 0
	v_pk_mul_f32 v[2:3], v[4:5], s[16:17] op_sel_hi:[1,0]
	s_nop 0
	v_med3_f32 v1, v2, s15, v212
	v_med3_f32 v2, v3, s15, v212
	v_cvt_pk_fp8_f32 v6, v1, v2 op_sel:[0,0,1]
	global_store_dword v190, v26, s[0:1]
	global_store_dword v190, v14, s[0:1] offset:256
	global_store_dword v190, v10, s[0:1] offset:512
	global_store_dword v190, v6, s[0:1] offset:768
